# s12 + BR: only the final (n=2) merged tile is stored write-through (sc1); intermediates stay plain
# speedup vs baseline: 1.0071x; 1.0071x over previous
;     __device__ __forceinline__ void operator()(const f32x4 (&acc)[2][2][4][2], const Unit& u, int wr, int wc, int fr, int fq) const {
;         const int row0 = u.pm * BM + wr * 64 + fr, col0 = u.pn * BM + wc * 32 + 8 * fq, n = u.z & 3;
;         h16* Gn = Gs + col0;
;         if ((u.z >> 2) == 0) {
; #pragma unroll
;             for (int ai = 0; ai < 2; ++ai)
; #pragma unroll
;                 for (int m = 0; m < 4; ++m) { h16* rowp = Gn + (size_t)(row0 + ai * HALF + m * 16) * ldg;
; #pragma unroll
;                     for (int bj = 0; bj < 2; ++bj) { f32x4 v0 = acc[ai][bj][m][0], v1 = acc[ai][bj][m][1];
; #pragma unroll
;                         for (int e = 0; e < 4; ++e) { v0[e] = __builtin_amdgcn_rcpf(1.f + __expf(-v0[e])); v1[e] = __builtin_amdgcn_rcpf(1.f + __expf(-v1[e])); }
;                         u32x4 w; w.x = cvt_pk_f16(v0[0], v0[1]); w.y = cvt_pk_f16(v0[2], v0[3]); w.z = cvt_pk_f16(v1[0], v1[1]); w.w = cvt_pk_f16(v1[2], v1[3]);
;                         *(u32x4*)(rowp + bj * HALF) = w; } }
;         } else {
; #pragma unroll
;             for (int ai = 0; ai < 2; ++ai)
; #pragma unroll
;                 for (int mp = 0; mp < 2; ++mp) {
;                     h16x8 gv[2][2], pv[2][2];
; #pragma unroll
;                     for (int mm = 0; mm < 2; ++mm)
; #pragma unroll
;                         for (int bj = 0; bj < 2; ++bj) { const size_t row = (size_t)(row0 + ai * HALF + (2 * mp + mm) * 16);
;                             gv[mm][bj] = *(const h16x8*)(Gn + row * ldg + bj * HALF);
;                             if (n > 0) pv[mm][bj] = *(const h16x8*)(Mg + row * 1024 + col0 + bj * HALF); }
; #pragma unroll
;                     for (int mm = 0; mm < 2; ++mm)
; #pragma unroll
;                         for (int bj = 0; bj < 2; ++bj) { const int m = 2 * mp + mm; const size_t row = (size_t)(row0 + ai * HALF + m * 16);
;                             float o[8];
; #pragma unroll
;                             for (int e = 0; e < 8; ++e) { const float a = e < 4 ? acc[ai][bj][m][0][e] : acc[ai][bj][m][1][e - 4]; o[e] = a * (float)gv[mm][bj][e]; }
;                             if (n > 0) {
; #pragma unroll
;                                 for (int e = 0; e < 8; ++e) o[e] += (float)pv[mm][bj][e]; }
;                             u32x4 w; w.x = cvt_pk_f16(o[0], o[1]); w.y = cvt_pk_f16(o[2], o[3]); w.z = cvt_pk_f16(o[4], o[5]); w.w = cvt_pk_f16(o[6], o[7]);
.LBB0_324:
	v_lshl_or_b32 v178, s73, 8, v165
	v_readlane_b32 s0, v253, 62
	v_ashrrev_i32_e32 v179, 31, v178
	v_readlane_b32 s1, v253, 63
	v_lshl_add_u32 v176, s75, 8, v192
	s_cmp_lt_u32 s72, 4
	v_lshl_add_u64 v[174:175], v[178:179], 1, s[0:1]
	s_mov_b64 s[0:1], -1
	s_cbranch_scc1 .LBB0_390
	s_and_b32 s0, s72, 3
	s_cmp_eq_u32 s0, 0
	s_cbranch_scc1 .Lbrepi_n0
	s_cmp_eq_u32 s0, 2
	s_cbranch_scc1 .Lbrepi_n2
	v_readlane_b32 s40, v254, 46
	v_readlane_b32 s41, v254, 47
	v_mov_b32_e32 v241, 0
	s_nop 1
	v_lshl_add_u64 v[180:181], v[178:179], 1, s[40:41]
	v_mov_b32_e32 v238, v176
	v_mad_i64_i32 v[234:235], s[0:1], v238, s91, v[174:175]
	v_lshlrev_b32_e32 v240, 11, v238
	v_lshl_add_u64 v[236:237], v[180:181], 0, v[240:241]
	global_load_dwordx4 v[130:133], v[234:235], off
	global_load_dwordx4 v[138:141], v[236:237], off
	global_load_dwordx4 v[134:137], v[234:235], off offset:256
	global_load_dwordx4 v[142:145], v[236:237], off offset:256
	v_add_u32_e32 v238, 16, v176
	v_mad_i64_i32 v[234:235], s[0:1], v238, s91, v[174:175]
	v_lshlrev_b32_e32 v240, 11, v238
	v_lshl_add_u64 v[236:237], v[180:181], 0, v[240:241]
	global_load_dwordx4 v[146:149], v[234:235], off
	global_load_dwordx4 v[154:157], v[236:237], off
	global_load_dwordx4 v[150:153], v[234:235], off offset:256
	global_load_dwordx4 v[158:161], v[236:237], off offset:256
	s_waitcnt vmcnt(4)
	v_mov_b32_e32 v238, v176
	v_lshlrev_b32_e32 v240, 11, v238
	v_lshl_add_u64 v[236:237], v[180:181], 0, v[240:241]
	v_cvt_f32_f16_e32 v182, v130
	v_cvt_f32_f16_sdwa v183, v130 dst_sel:DWORD dst_unused:UNUSED_PAD src0_sel:WORD_1
	v_cvt_f32_f16_e32 v184, v131
	v_cvt_f32_f16_sdwa v185, v131 dst_sel:DWORD dst_unused:UNUSED_PAD src0_sel:WORD_1
	v_cvt_f32_f16_e32 v186, v132
	v_cvt_f32_f16_sdwa v187, v132 dst_sel:DWORD dst_unused:UNUSED_PAD src0_sel:WORD_1
	v_cvt_f32_f16_e32 v188, v133
	v_cvt_f32_f16_sdwa v189, v133 dst_sel:DWORD dst_unused:UNUSED_PAD src0_sel:WORD_1
	v_cvt_f32_f16_e32 v196, v138
	v_cvt_f32_f16_sdwa v197, v138 dst_sel:DWORD dst_unused:UNUSED_PAD src0_sel:WORD_1
	v_cvt_f32_f16_e32 v198, v139
	v_cvt_f32_f16_sdwa v199, v139 dst_sel:DWORD dst_unused:UNUSED_PAD src0_sel:WORD_1
	v_cvt_f32_f16_e32 v200, v140
	v_cvt_f32_f16_sdwa v201, v140 dst_sel:DWORD dst_unused:UNUSED_PAD src0_sel:WORD_1
	v_cvt_f32_f16_e32 v202, v141
	v_cvt_f32_f16_sdwa v203, v141 dst_sel:DWORD dst_unused:UNUSED_PAD src0_sel:WORD_1
	v_pk_mul_f32 v[182:183], v[126:127], v[182:183]
	v_pk_mul_f32 v[184:185], v[128:129], v[184:185]
	v_pk_mul_f32 v[186:187], v[122:123], v[186:187]
	v_pk_mul_f32 v[188:189], v[124:125], v[188:189]
	v_pk_add_f32 v[182:183], v[182:183], v[196:197]
	v_pk_add_f32 v[184:185], v[184:185], v[198:199]
	v_pk_add_f32 v[186:187], v[186:187], v[200:201]
	v_pk_add_f32 v[188:189], v[188:189], v[202:203]
	v_cvt_pk_f16_f32 v126, v182, v183
	v_cvt_pk_f16_f32 v127, v184, v185
	v_cvt_pk_f16_f32 v128, v186, v187
	v_cvt_pk_f16_f32 v129, v188, v189
	global_store_dwordx4 v[236:237], v[126:129], off
	v_cvt_f32_f16_e32 v182, v134
	v_cvt_f32_f16_sdwa v183, v134 dst_sel:DWORD dst_unused:UNUSED_PAD src0_sel:WORD_1
	v_cvt_f32_f16_e32 v184, v135
	v_cvt_f32_f16_sdwa v185, v135 dst_sel:DWORD dst_unused:UNUSED_PAD src0_sel:WORD_1
	v_cvt_f32_f16_e32 v186, v136
	v_cvt_f32_f16_sdwa v187, v136 dst_sel:DWORD dst_unused:UNUSED_PAD src0_sel:WORD_1
	v_cvt_f32_f16_e32 v188, v137
	v_cvt_f32_f16_sdwa v189, v137 dst_sel:DWORD dst_unused:UNUSED_PAD src0_sel:WORD_1
	v_cvt_f32_f16_e32 v196, v142
	v_cvt_f32_f16_sdwa v197, v142 dst_sel:DWORD dst_unused:UNUSED_PAD src0_sel:WORD_1
	v_cvt_f32_f16_e32 v198, v143
	v_cvt_f32_f16_sdwa v199, v143 dst_sel:DWORD dst_unused:UNUSED_PAD src0_sel:WORD_1
	v_cvt_f32_f16_e32 v200, v144
	v_cvt_f32_f16_sdwa v201, v144 dst_sel:DWORD dst_unused:UNUSED_PAD src0_sel:WORD_1
	v_cvt_f32_f16_e32 v202, v145
	v_cvt_f32_f16_sdwa v203, v145 dst_sel:DWORD dst_unused:UNUSED_PAD src0_sel:WORD_1
	v_pk_mul_f32 v[182:183], v[118:119], v[182:183]
	v_pk_mul_f32 v[184:185], v[120:121], v[184:185]
	v_pk_mul_f32 v[186:187], v[114:115], v[186:187]
	v_pk_mul_f32 v[188:189], v[116:117], v[188:189]
	v_pk_add_f32 v[182:183], v[182:183], v[196:197]
	v_pk_add_f32 v[184:185], v[184:185], v[198:199]
	v_pk_add_f32 v[186:187], v[186:187], v[200:201]
	v_pk_add_f32 v[188:189], v[188:189], v[202:203]
	v_cvt_pk_f16_f32 v118, v182, v183
	v_cvt_pk_f16_f32 v119, v184, v185
	v_cvt_pk_f16_f32 v120, v186, v187
	v_cvt_pk_f16_f32 v121, v188, v189
	global_store_dwordx4 v[236:237], v[118:121], off offset:256
	v_add_u32_e32 v238, 32, v176
	v_mad_i64_i32 v[234:235], s[0:1], v238, s91, v[174:175]
	v_lshlrev_b32_e32 v240, 11, v238
	v_lshl_add_u64 v[236:237], v[180:181], 0, v[240:241]
	global_load_dwordx4 v[130:133], v[234:235], off
	global_load_dwordx4 v[138:141], v[236:237], off
	global_load_dwordx4 v[134:137], v[234:235], off offset:256
	global_load_dwordx4 v[142:145], v[236:237], off offset:256
	s_nop 1
	v_add_u32_e32 v238, 48, v176
	v_mad_i64_i32 v[234:235], s[0:1], v238, s91, v[174:175]
	v_lshlrev_b32_e32 v240, 11, v238
	v_lshl_add_u64 v[236:237], v[180:181], 0, v[240:241]
	global_load_dwordx4 v[126:129], v[234:235], off
	global_load_dwordx4 v[118:121], v[236:237], off
	global_load_dwordx4 v[122:125], v[234:235], off offset:256
	global_load_dwordx4 v[114:117], v[236:237], off offset:256
	s_waitcnt vmcnt(10)
; __device__ __forceinline__ unsigned cvt_pk_f16(float lo, float hi) { f32x2 v = {lo, hi}; h16x2 b = __builtin_convertvector(v, h16x2); return __builtin_bit_cast(unsigned, b); }
;     __device__ __forceinline__ void operator()(const f32x4 (&acc)[2][2][4][2], const Unit& u, int wr, int wc, int fr, int fq) const {
;     ...
;                         for (int bj = 0; bj < 2; ++bj) { const size_t row = (size_t)(row0 + ai * HALF + (2 * mp + mm) * 16);
;                             gv[mm][bj] = *(const h16x8*)(Gn + row * ldg + bj * HALF);
;                             if (n > 0) pv[mm][bj] = *(const h16x8*)(Mg + row * 1024 + col0 + bj * HALF); }
; #pragma unroll
;                     for (int mm = 0; mm < 2; ++mm)
; #pragma unroll
;                         for (int bj = 0; bj < 2; ++bj) { const int m = 2 * mp + mm; const size_t row = (size_t)(row0 + ai * HALF + m * 16);
;                             float o[8];
; #pragma unroll
;                             for (int e = 0; e < 8; ++e) { const float a = e < 4 ? acc[ai][bj][m][0][e] : acc[ai][bj][m][1][e - 4]; o[e] = a * (float)gv[mm][bj][e]; }
;                             if (n > 0) {
; #pragma unroll
;                                 for (int e = 0; e < 8; ++e) o[e] += (float)pv[mm][bj][e]; }
;                             u32x4 w; w.x = cvt_pk_f16(o[0], o[1]); w.y = cvt_pk_f16(o[2], o[3]); w.z = cvt_pk_f16(o[4], o[5]); w.w = cvt_pk_f16(o[6], o[7]);
;                             *(u32x4*)(Mg + row * 1024 + col0 + bj * HALF) = w; }
	v_add_u32_e32 v238, 16, v176
	v_lshlrev_b32_e32 v240, 11, v238
	v_lshl_add_u64 v[236:237], v[180:181], 0, v[240:241]
	v_cvt_f32_f16_e32 v182, v146
	v_cvt_f32_f16_sdwa v183, v146 dst_sel:DWORD dst_unused:UNUSED_PAD src0_sel:WORD_1
	v_cvt_f32_f16_e32 v184, v147
	v_cvt_f32_f16_sdwa v185, v147 dst_sel:DWORD dst_unused:UNUSED_PAD src0_sel:WORD_1
	v_cvt_f32_f16_e32 v186, v148
	v_cvt_f32_f16_sdwa v187, v148 dst_sel:DWORD dst_unused:UNUSED_PAD src0_sel:WORD_1
	v_cvt_f32_f16_e32 v188, v149
	v_cvt_f32_f16_sdwa v189, v149 dst_sel:DWORD dst_unused:UNUSED_PAD src0_sel:WORD_1
	v_cvt_f32_f16_e32 v196, v154
	v_cvt_f32_f16_sdwa v197, v154 dst_sel:DWORD dst_unused:UNUSED_PAD src0_sel:WORD_1
	v_cvt_f32_f16_e32 v198, v155
	v_cvt_f32_f16_sdwa v199, v155 dst_sel:DWORD dst_unused:UNUSED_PAD src0_sel:WORD_1
	v_cvt_f32_f16_e32 v200, v156
	v_cvt_f32_f16_sdwa v201, v156 dst_sel:DWORD dst_unused:UNUSED_PAD src0_sel:WORD_1
	v_cvt_f32_f16_e32 v202, v157
	v_cvt_f32_f16_sdwa v203, v157 dst_sel:DWORD dst_unused:UNUSED_PAD src0_sel:WORD_1
	v_pk_mul_f32 v[182:183], v[110:111], v[182:183]
	v_pk_mul_f32 v[184:185], v[112:113], v[184:185]
	v_pk_mul_f32 v[186:187], v[106:107], v[186:187]
	v_pk_mul_f32 v[188:189], v[108:109], v[188:189]
	v_pk_add_f32 v[182:183], v[182:183], v[196:197]
	v_pk_add_f32 v[184:185], v[184:185], v[198:199]
	v_pk_add_f32 v[186:187], v[186:187], v[200:201]
	v_pk_add_f32 v[188:189], v[188:189], v[202:203]
	v_cvt_pk_f16_f32 v110, v182, v183
	v_cvt_pk_f16_f32 v111, v184, v185
	v_cvt_pk_f16_f32 v112, v186, v187
	v_cvt_pk_f16_f32 v113, v188, v189
	global_store_dwordx4 v[236:237], v[110:113], off
	v_cvt_f32_f16_e32 v182, v150
	v_cvt_f32_f16_sdwa v183, v150 dst_sel:DWORD dst_unused:UNUSED_PAD src0_sel:WORD_1
	v_cvt_f32_f16_e32 v184, v151
	v_cvt_f32_f16_sdwa v185, v151 dst_sel:DWORD dst_unused:UNUSED_PAD src0_sel:WORD_1
	v_cvt_f32_f16_e32 v186, v152
	v_cvt_f32_f16_sdwa v187, v152 dst_sel:DWORD dst_unused:UNUSED_PAD src0_sel:WORD_1
	v_cvt_f32_f16_e32 v188, v153
	v_cvt_f32_f16_sdwa v189, v153 dst_sel:DWORD dst_unused:UNUSED_PAD src0_sel:WORD_1
	v_cvt_f32_f16_e32 v196, v158
	v_cvt_f32_f16_sdwa v197, v158 dst_sel:DWORD dst_unused:UNUSED_PAD src0_sel:WORD_1
	v_cvt_f32_f16_e32 v198, v159
	v_cvt_f32_f16_sdwa v199, v159 dst_sel:DWORD dst_unused:UNUSED_PAD src0_sel:WORD_1
	v_cvt_f32_f16_e32 v200, v160
	v_cvt_f32_f16_sdwa v201, v160 dst_sel:DWORD dst_unused:UNUSED_PAD src0_sel:WORD_1
	v_cvt_f32_f16_e32 v202, v161
	v_cvt_f32_f16_sdwa v203, v161 dst_sel:DWORD dst_unused:UNUSED_PAD src0_sel:WORD_1
	v_pk_mul_f32 v[182:183], v[102:103], v[182:183]
	v_pk_mul_f32 v[184:185], v[104:105], v[184:185]
	v_pk_mul_f32 v[186:187], v[98:99], v[186:187]
	v_pk_mul_f32 v[188:189], v[100:101], v[188:189]
	v_pk_add_f32 v[182:183], v[182:183], v[196:197]
	v_pk_add_f32 v[184:185], v[184:185], v[198:199]
	v_pk_add_f32 v[186:187], v[186:187], v[200:201]
	v_pk_add_f32 v[188:189], v[188:189], v[202:203]
	v_cvt_pk_f16_f32 v102, v182, v183
	v_cvt_pk_f16_f32 v103, v184, v185
	v_cvt_pk_f16_f32 v104, v186, v187
	v_cvt_pk_f16_f32 v105, v188, v189
	global_store_dwordx4 v[236:237], v[102:105], off offset:256
	v_add_u32_e32 v238, 128, v176
	v_mad_i64_i32 v[234:235], s[0:1], v238, s91, v[174:175]
	v_lshlrev_b32_e32 v240, 11, v238
	v_lshl_add_u64 v[236:237], v[180:181], 0, v[240:241]
	global_load_dwordx4 v[146:149], v[234:235], off
	global_load_dwordx4 v[154:157], v[236:237], off
	global_load_dwordx4 v[150:153], v[234:235], off offset:256
	global_load_dwordx4 v[158:161], v[236:237], off offset:256
	s_nop 1
	v_add_u32_e32 v238, 144, v176
	v_mad_i64_i32 v[234:235], s[0:1], v238, s91, v[174:175]
	v_lshlrev_b32_e32 v240, 11, v238
	v_lshl_add_u64 v[236:237], v[180:181], 0, v[240:241]
	global_load_dwordx4 v[110:113], v[234:235], off
	global_load_dwordx4 v[102:105], v[236:237], off
	global_load_dwordx4 v[106:109], v[234:235], off offset:256
	global_load_dwordx4 v[98:101], v[236:237], off offset:256
	s_waitcnt vmcnt(14)
	v_add_u32_e32 v238, 32, v176
	v_lshlrev_b32_e32 v240, 11, v238
	v_lshl_add_u64 v[236:237], v[180:181], 0, v[240:241]
	v_cvt_f32_f16_e32 v182, v130
	v_cvt_f32_f16_sdwa v183, v130 dst_sel:DWORD dst_unused:UNUSED_PAD src0_sel:WORD_1
	v_cvt_f32_f16_e32 v184, v131
	v_cvt_f32_f16_sdwa v185, v131 dst_sel:DWORD dst_unused:UNUSED_PAD src0_sel:WORD_1
	v_cvt_f32_f16_e32 v186, v132
	v_cvt_f32_f16_sdwa v187, v132 dst_sel:DWORD dst_unused:UNUSED_PAD src0_sel:WORD_1
	v_cvt_f32_f16_e32 v188, v133
	v_cvt_f32_f16_sdwa v189, v133 dst_sel:DWORD dst_unused:UNUSED_PAD src0_sel:WORD_1
	v_cvt_f32_f16_e32 v196, v138
	v_cvt_f32_f16_sdwa v197, v138 dst_sel:DWORD dst_unused:UNUSED_PAD src0_sel:WORD_1
	v_cvt_f32_f16_e32 v198, v139
	v_cvt_f32_f16_sdwa v199, v139 dst_sel:DWORD dst_unused:UNUSED_PAD src0_sel:WORD_1
	v_cvt_f32_f16_e32 v200, v140
	v_cvt_f32_f16_sdwa v201, v140 dst_sel:DWORD dst_unused:UNUSED_PAD src0_sel:WORD_1
	v_cvt_f32_f16_e32 v202, v141
	v_cvt_f32_f16_sdwa v203, v141 dst_sel:DWORD dst_unused:UNUSED_PAD src0_sel:WORD_1
	v_pk_mul_f32 v[182:183], v[92:93], v[182:183]
	v_pk_mul_f32 v[184:185], v[94:95], v[184:185]
	v_pk_mul_f32 v[186:187], v[88:89], v[186:187]
	v_pk_mul_f32 v[188:189], v[90:91], v[188:189]
	v_pk_add_f32 v[182:183], v[182:183], v[196:197]
	v_pk_add_f32 v[184:185], v[184:185], v[198:199]
	v_pk_add_f32 v[186:187], v[186:187], v[200:201]
	v_pk_add_f32 v[188:189], v[188:189], v[202:203]
	v_cvt_pk_f16_f32 v92, v182, v183
	v_cvt_pk_f16_f32 v93, v184, v185
	v_cvt_pk_f16_f32 v94, v186, v187
	v_cvt_pk_f16_f32 v95, v188, v189
	global_store_dwordx4 v[236:237], v[92:95], off
	v_cvt_f32_f16_e32 v182, v134
	v_cvt_f32_f16_sdwa v183, v134 dst_sel:DWORD dst_unused:UNUSED_PAD src0_sel:WORD_1
	v_cvt_f32_f16_e32 v184, v135
; __device__ __forceinline__ unsigned cvt_pk_f16(float lo, float hi) { f32x2 v = {lo, hi}; h16x2 b = __builtin_convertvector(v, h16x2); return __builtin_bit_cast(unsigned, b); }
;     __device__ __forceinline__ void operator()(const f32x4 (&acc)[2][2][4][2], const Unit& u, int wr, int wc, int fr, int fq) const {
;     ...
;                         for (int bj = 0; bj < 2; ++bj) { const size_t row = (size_t)(row0 + ai * HALF + (2 * mp + mm) * 16);
;                             gv[mm][bj] = *(const h16x8*)(Gn + row * ldg + bj * HALF);
;                             if (n > 0) pv[mm][bj] = *(const h16x8*)(Mg + row * 1024 + col0 + bj * HALF); }
; #pragma unroll
;                     for (int mm = 0; mm < 2; ++mm)
; #pragma unroll
;                         for (int bj = 0; bj < 2; ++bj) { const int m = 2 * mp + mm; const size_t row = (size_t)(row0 + ai * HALF + m * 16);
;                             float o[8];
; #pragma unroll
;                             for (int e = 0; e < 8; ++e) { const float a = e < 4 ? acc[ai][bj][m][0][e] : acc[ai][bj][m][1][e - 4]; o[e] = a * (float)gv[mm][bj][e]; }
;                             if (n > 0) {
; #pragma unroll
;                                 for (int e = 0; e < 8; ++e) o[e] += (float)pv[mm][bj][e]; }
;                             u32x4 w; w.x = cvt_pk_f16(o[0], o[1]); w.y = cvt_pk_f16(o[2], o[3]); w.z = cvt_pk_f16(o[4], o[5]); w.w = cvt_pk_f16(o[6], o[7]);
;                             *(u32x4*)(Mg + row * 1024 + col0 + bj * HALF) = w; }
	v_cvt_f32_f16_sdwa v185, v135 dst_sel:DWORD dst_unused:UNUSED_PAD src0_sel:WORD_1
	v_cvt_f32_f16_e32 v186, v136
	v_cvt_f32_f16_sdwa v187, v136 dst_sel:DWORD dst_unused:UNUSED_PAD src0_sel:WORD_1
	v_cvt_f32_f16_e32 v188, v137
	v_cvt_f32_f16_sdwa v189, v137 dst_sel:DWORD dst_unused:UNUSED_PAD src0_sel:WORD_1
	v_cvt_f32_f16_e32 v196, v142
	v_cvt_f32_f16_sdwa v197, v142 dst_sel:DWORD dst_unused:UNUSED_PAD src0_sel:WORD_1
	v_cvt_f32_f16_e32 v198, v143
	v_cvt_f32_f16_sdwa v199, v143 dst_sel:DWORD dst_unused:UNUSED_PAD src0_sel:WORD_1
	v_cvt_f32_f16_e32 v200, v144
	v_cvt_f32_f16_sdwa v201, v144 dst_sel:DWORD dst_unused:UNUSED_PAD src0_sel:WORD_1
	v_cvt_f32_f16_e32 v202, v145
	v_cvt_f32_f16_sdwa v203, v145 dst_sel:DWORD dst_unused:UNUSED_PAD src0_sel:WORD_1
	v_pk_mul_f32 v[182:183], v[84:85], v[182:183]
	v_pk_mul_f32 v[184:185], v[86:87], v[184:185]
	v_pk_mul_f32 v[186:187], v[80:81], v[186:187]
	v_pk_mul_f32 v[188:189], v[82:83], v[188:189]
	v_pk_add_f32 v[182:183], v[182:183], v[196:197]
	v_pk_add_f32 v[184:185], v[184:185], v[198:199]
	v_pk_add_f32 v[186:187], v[186:187], v[200:201]
	v_pk_add_f32 v[188:189], v[188:189], v[202:203]
	v_cvt_pk_f16_f32 v84, v182, v183
	v_cvt_pk_f16_f32 v85, v184, v185
	v_cvt_pk_f16_f32 v86, v186, v187
	v_cvt_pk_f16_f32 v87, v188, v189
	global_store_dwordx4 v[236:237], v[84:87], off offset:256
	v_add_u32_e32 v238, 160, v176
	v_mad_i64_i32 v[234:235], s[0:1], v238, s91, v[174:175]
	v_lshlrev_b32_e32 v240, 11, v238
	v_lshl_add_u64 v[236:237], v[180:181], 0, v[240:241]
	global_load_dwordx4 v[130:133], v[234:235], off
	global_load_dwordx4 v[138:141], v[236:237], off
	global_load_dwordx4 v[134:137], v[234:235], off offset:256
	global_load_dwordx4 v[142:145], v[236:237], off offset:256
	s_nop 1
	v_add_u32_e32 v238, 176, v176
	v_mad_i64_i32 v[234:235], s[0:1], v238, s91, v[174:175]
	v_lshlrev_b32_e32 v240, 11, v238
	v_lshl_add_u64 v[236:237], v[180:181], 0, v[240:241]
	global_load_dwordx4 v[92:95], v[234:235], off
	global_load_dwordx4 v[84:87], v[236:237], off
	global_load_dwordx4 v[88:91], v[234:235], off offset:256
	global_load_dwordx4 v[80:83], v[236:237], off offset:256
	s_waitcnt vmcnt(20)
	v_add_u32_e32 v238, 48, v176
	v_lshlrev_b32_e32 v240, 11, v238
	v_lshl_add_u64 v[236:237], v[180:181], 0, v[240:241]
	v_cvt_f32_f16_e32 v182, v126
	v_cvt_f32_f16_sdwa v183, v126 dst_sel:DWORD dst_unused:UNUSED_PAD src0_sel:WORD_1
	v_cvt_f32_f16_e32 v184, v127
	v_cvt_f32_f16_sdwa v185, v127 dst_sel:DWORD dst_unused:UNUSED_PAD src0_sel:WORD_1
	v_cvt_f32_f16_e32 v186, v128
	v_cvt_f32_f16_sdwa v187, v128 dst_sel:DWORD dst_unused:UNUSED_PAD src0_sel:WORD_1
	v_cvt_f32_f16_e32 v188, v129
	v_cvt_f32_f16_sdwa v189, v129 dst_sel:DWORD dst_unused:UNUSED_PAD src0_sel:WORD_1
	v_cvt_f32_f16_e32 v196, v118
	v_cvt_f32_f16_sdwa v197, v118 dst_sel:DWORD dst_unused:UNUSED_PAD src0_sel:WORD_1
	v_cvt_f32_f16_e32 v198, v119
	v_cvt_f32_f16_sdwa v199, v119 dst_sel:DWORD dst_unused:UNUSED_PAD src0_sel:WORD_1
	v_cvt_f32_f16_e32 v200, v120
	v_cvt_f32_f16_sdwa v201, v120 dst_sel:DWORD dst_unused:UNUSED_PAD src0_sel:WORD_1
	v_cvt_f32_f16_e32 v202, v121
	v_cvt_f32_f16_sdwa v203, v121 dst_sel:DWORD dst_unused:UNUSED_PAD src0_sel:WORD_1
	v_pk_mul_f32 v[182:183], v[76:77], v[182:183]
	v_pk_mul_f32 v[184:185], v[78:79], v[184:185]
	v_pk_mul_f32 v[186:187], v[72:73], v[186:187]
	v_pk_mul_f32 v[188:189], v[74:75], v[188:189]
	v_pk_add_f32 v[182:183], v[182:183], v[196:197]
	v_pk_add_f32 v[184:185], v[184:185], v[198:199]
	v_pk_add_f32 v[186:187], v[186:187], v[200:201]
	v_pk_add_f32 v[188:189], v[188:189], v[202:203]
	v_cvt_pk_f16_f32 v76, v182, v183
	v_cvt_pk_f16_f32 v77, v184, v185
	v_cvt_pk_f16_f32 v78, v186, v187
	v_cvt_pk_f16_f32 v79, v188, v189
	global_store_dwordx4 v[236:237], v[76:79], off
	v_cvt_f32_f16_e32 v182, v122
	v_cvt_f32_f16_sdwa v183, v122 dst_sel:DWORD dst_unused:UNUSED_PAD src0_sel:WORD_1
	v_cvt_f32_f16_e32 v184, v123
	v_cvt_f32_f16_sdwa v185, v123 dst_sel:DWORD dst_unused:UNUSED_PAD src0_sel:WORD_1
	v_cvt_f32_f16_e32 v186, v124
	v_cvt_f32_f16_sdwa v187, v124 dst_sel:DWORD dst_unused:UNUSED_PAD src0_sel:WORD_1
	v_cvt_f32_f16_e32 v188, v125
	v_cvt_f32_f16_sdwa v189, v125 dst_sel:DWORD dst_unused:UNUSED_PAD src0_sel:WORD_1
	v_cvt_f32_f16_e32 v196, v114
	v_cvt_f32_f16_sdwa v197, v114 dst_sel:DWORD dst_unused:UNUSED_PAD src0_sel:WORD_1
	v_cvt_f32_f16_e32 v198, v115
	v_cvt_f32_f16_sdwa v199, v115 dst_sel:DWORD dst_unused:UNUSED_PAD src0_sel:WORD_1
	v_cvt_f32_f16_e32 v200, v116
	v_cvt_f32_f16_sdwa v201, v116 dst_sel:DWORD dst_unused:UNUSED_PAD src0_sel:WORD_1
	v_cvt_f32_f16_e32 v202, v117
	v_cvt_f32_f16_sdwa v203, v117 dst_sel:DWORD dst_unused:UNUSED_PAD src0_sel:WORD_1
	v_pk_mul_f32 v[182:183], v[68:69], v[182:183]
	v_pk_mul_f32 v[184:185], v[70:71], v[184:185]
	v_pk_mul_f32 v[186:187], v[64:65], v[186:187]
	v_pk_mul_f32 v[188:189], v[66:67], v[188:189]
	v_pk_add_f32 v[182:183], v[182:183], v[196:197]
	v_pk_add_f32 v[184:185], v[184:185], v[198:199]
	v_pk_add_f32 v[186:187], v[186:187], v[200:201]
	v_pk_add_f32 v[188:189], v[188:189], v[202:203]
	v_cvt_pk_f16_f32 v68, v182, v183
	v_cvt_pk_f16_f32 v69, v184, v185
	v_cvt_pk_f16_f32 v70, v186, v187
	v_cvt_pk_f16_f32 v71, v188, v189
	global_store_dwordx4 v[236:237], v[68:71], off offset:256
	s_waitcnt vmcnt(16)
; __device__ __forceinline__ unsigned cvt_pk_f16(float lo, float hi) { f32x2 v = {lo, hi}; h16x2 b = __builtin_convertvector(v, h16x2); return __builtin_bit_cast(unsigned, b); }
;     __device__ __forceinline__ void operator()(const f32x4 (&acc)[2][2][4][2], const Unit& u, int wr, int wc, int fr, int fq) const {
;     ...
;                         for (int bj = 0; bj < 2; ++bj) { const size_t row = (size_t)(row0 + ai * HALF + (2 * mp + mm) * 16);
;                             gv[mm][bj] = *(const h16x8*)(Gn + row * ldg + bj * HALF);
;                             if (n > 0) pv[mm][bj] = *(const h16x8*)(Mg + row * 1024 + col0 + bj * HALF); }
; #pragma unroll
;                     for (int mm = 0; mm < 2; ++mm)
; #pragma unroll
;                         for (int bj = 0; bj < 2; ++bj) { const int m = 2 * mp + mm; const size_t row = (size_t)(row0 + ai * HALF + m * 16);
;                             float o[8];
; #pragma unroll
;                             for (int e = 0; e < 8; ++e) { const float a = e < 4 ? acc[ai][bj][m][0][e] : acc[ai][bj][m][1][e - 4]; o[e] = a * (float)gv[mm][bj][e]; }
;                             if (n > 0) {
; #pragma unroll
;                                 for (int e = 0; e < 8; ++e) o[e] += (float)pv[mm][bj][e]; }
;                             u32x4 w; w.x = cvt_pk_f16(o[0], o[1]); w.y = cvt_pk_f16(o[2], o[3]); w.z = cvt_pk_f16(o[4], o[5]); w.w = cvt_pk_f16(o[6], o[7]);
;                             *(u32x4*)(Mg + row * 1024 + col0 + bj * HALF) = w; }
	v_add_u32_e32 v238, 128, v176
	v_lshlrev_b32_e32 v240, 11, v238
	v_lshl_add_u64 v[236:237], v[180:181], 0, v[240:241]
	v_cvt_f32_f16_e32 v182, v146
	v_cvt_f32_f16_sdwa v183, v146 dst_sel:DWORD dst_unused:UNUSED_PAD src0_sel:WORD_1
	v_cvt_f32_f16_e32 v184, v147
	v_cvt_f32_f16_sdwa v185, v147 dst_sel:DWORD dst_unused:UNUSED_PAD src0_sel:WORD_1
	v_cvt_f32_f16_e32 v186, v148
	v_cvt_f32_f16_sdwa v187, v148 dst_sel:DWORD dst_unused:UNUSED_PAD src0_sel:WORD_1
	v_cvt_f32_f16_e32 v188, v149
	v_cvt_f32_f16_sdwa v189, v149 dst_sel:DWORD dst_unused:UNUSED_PAD src0_sel:WORD_1
	v_cvt_f32_f16_e32 v196, v154
	v_cvt_f32_f16_sdwa v197, v154 dst_sel:DWORD dst_unused:UNUSED_PAD src0_sel:WORD_1
	v_cvt_f32_f16_e32 v198, v155
	v_cvt_f32_f16_sdwa v199, v155 dst_sel:DWORD dst_unused:UNUSED_PAD src0_sel:WORD_1
	v_cvt_f32_f16_e32 v200, v156
	v_cvt_f32_f16_sdwa v201, v156 dst_sel:DWORD dst_unused:UNUSED_PAD src0_sel:WORD_1
	v_cvt_f32_f16_e32 v202, v157
	v_cvt_f32_f16_sdwa v203, v157 dst_sel:DWORD dst_unused:UNUSED_PAD src0_sel:WORD_1
	v_pk_mul_f32 v[182:183], v[60:61], v[182:183]
	v_pk_mul_f32 v[184:185], v[62:63], v[184:185]
	v_pk_mul_f32 v[186:187], v[56:57], v[186:187]
	v_pk_mul_f32 v[188:189], v[58:59], v[188:189]
	v_pk_add_f32 v[182:183], v[182:183], v[196:197]
	v_pk_add_f32 v[184:185], v[184:185], v[198:199]
	v_pk_add_f32 v[186:187], v[186:187], v[200:201]
	v_pk_add_f32 v[188:189], v[188:189], v[202:203]
	v_cvt_pk_f16_f32 v60, v182, v183
	v_cvt_pk_f16_f32 v61, v184, v185
	v_cvt_pk_f16_f32 v62, v186, v187
	v_cvt_pk_f16_f32 v63, v188, v189
	global_store_dwordx4 v[236:237], v[60:63], off
	v_cvt_f32_f16_e32 v182, v150
	v_cvt_f32_f16_sdwa v183, v150 dst_sel:DWORD dst_unused:UNUSED_PAD src0_sel:WORD_1
	v_cvt_f32_f16_e32 v184, v151
	v_cvt_f32_f16_sdwa v185, v151 dst_sel:DWORD dst_unused:UNUSED_PAD src0_sel:WORD_1
	v_cvt_f32_f16_e32 v186, v152
	v_cvt_f32_f16_sdwa v187, v152 dst_sel:DWORD dst_unused:UNUSED_PAD src0_sel:WORD_1
	v_cvt_f32_f16_e32 v188, v153
	v_cvt_f32_f16_sdwa v189, v153 dst_sel:DWORD dst_unused:UNUSED_PAD src0_sel:WORD_1
	v_cvt_f32_f16_e32 v196, v158
	v_cvt_f32_f16_sdwa v197, v158 dst_sel:DWORD dst_unused:UNUSED_PAD src0_sel:WORD_1
	v_cvt_f32_f16_e32 v198, v159
	v_cvt_f32_f16_sdwa v199, v159 dst_sel:DWORD dst_unused:UNUSED_PAD src0_sel:WORD_1
	v_cvt_f32_f16_e32 v200, v160
	v_cvt_f32_f16_sdwa v201, v160 dst_sel:DWORD dst_unused:UNUSED_PAD src0_sel:WORD_1
	v_cvt_f32_f16_e32 v202, v161
	v_cvt_f32_f16_sdwa v203, v161 dst_sel:DWORD dst_unused:UNUSED_PAD src0_sel:WORD_1
	v_pk_mul_f32 v[182:183], v[52:53], v[182:183]
	v_pk_mul_f32 v[184:185], v[54:55], v[184:185]
	v_pk_mul_f32 v[186:187], v[48:49], v[186:187]
	v_pk_mul_f32 v[188:189], v[50:51], v[188:189]
	v_pk_add_f32 v[182:183], v[182:183], v[196:197]
	v_pk_add_f32 v[184:185], v[184:185], v[198:199]
	v_pk_add_f32 v[186:187], v[186:187], v[200:201]
	v_pk_add_f32 v[188:189], v[188:189], v[202:203]
	v_cvt_pk_f16_f32 v52, v182, v183
	v_cvt_pk_f16_f32 v53, v184, v185
	v_cvt_pk_f16_f32 v54, v186, v187
	v_cvt_pk_f16_f32 v55, v188, v189
	global_store_dwordx4 v[236:237], v[52:55], off offset:256
	s_waitcnt vmcnt(14)
	v_add_u32_e32 v238, 144, v176
	v_lshlrev_b32_e32 v240, 11, v238
	v_lshl_add_u64 v[236:237], v[180:181], 0, v[240:241]
	v_cvt_f32_f16_e32 v182, v110
	v_cvt_f32_f16_sdwa v183, v110 dst_sel:DWORD dst_unused:UNUSED_PAD src0_sel:WORD_1
	v_cvt_f32_f16_e32 v184, v111
	v_cvt_f32_f16_sdwa v185, v111 dst_sel:DWORD dst_unused:UNUSED_PAD src0_sel:WORD_1
	v_cvt_f32_f16_e32 v186, v112
	v_cvt_f32_f16_sdwa v187, v112 dst_sel:DWORD dst_unused:UNUSED_PAD src0_sel:WORD_1
	v_cvt_f32_f16_e32 v188, v113
	v_cvt_f32_f16_sdwa v189, v113 dst_sel:DWORD dst_unused:UNUSED_PAD src0_sel:WORD_1
	v_cvt_f32_f16_e32 v196, v102
	v_cvt_f32_f16_sdwa v197, v102 dst_sel:DWORD dst_unused:UNUSED_PAD src0_sel:WORD_1
	v_cvt_f32_f16_e32 v198, v103
	v_cvt_f32_f16_sdwa v199, v103 dst_sel:DWORD dst_unused:UNUSED_PAD src0_sel:WORD_1
	v_cvt_f32_f16_e32 v200, v104
	v_cvt_f32_f16_sdwa v201, v104 dst_sel:DWORD dst_unused:UNUSED_PAD src0_sel:WORD_1
	v_cvt_f32_f16_e32 v202, v105
	v_cvt_f32_f16_sdwa v203, v105 dst_sel:DWORD dst_unused:UNUSED_PAD src0_sel:WORD_1
	v_pk_mul_f32 v[182:183], v[44:45], v[182:183]
	v_pk_mul_f32 v[184:185], v[46:47], v[184:185]
	v_pk_mul_f32 v[186:187], v[40:41], v[186:187]
	v_pk_mul_f32 v[188:189], v[42:43], v[188:189]
	v_pk_add_f32 v[182:183], v[182:183], v[196:197]
	v_pk_add_f32 v[184:185], v[184:185], v[198:199]
	v_pk_add_f32 v[186:187], v[186:187], v[200:201]
	v_pk_add_f32 v[188:189], v[188:189], v[202:203]
	v_cvt_pk_f16_f32 v44, v182, v183
	v_cvt_pk_f16_f32 v45, v184, v185
	v_cvt_pk_f16_f32 v46, v186, v187
	v_cvt_pk_f16_f32 v47, v188, v189
	global_store_dwordx4 v[236:237], v[44:47], off
	v_cvt_f32_f16_e32 v182, v106
	v_cvt_f32_f16_sdwa v183, v106 dst_sel:DWORD dst_unused:UNUSED_PAD src0_sel:WORD_1
	v_cvt_f32_f16_e32 v184, v107
	v_cvt_f32_f16_sdwa v185, v107 dst_sel:DWORD dst_unused:UNUSED_PAD src0_sel:WORD_1
	v_cvt_f32_f16_e32 v186, v108
	v_cvt_f32_f16_sdwa v187, v108 dst_sel:DWORD dst_unused:UNUSED_PAD src0_sel:WORD_1
	v_cvt_f32_f16_e32 v188, v109
	v_cvt_f32_f16_sdwa v189, v109 dst_sel:DWORD dst_unused:UNUSED_PAD src0_sel:WORD_1
	v_cvt_f32_f16_e32 v196, v98
	v_cvt_f32_f16_sdwa v197, v98 dst_sel:DWORD dst_unused:UNUSED_PAD src0_sel:WORD_1
	v_cvt_f32_f16_e32 v198, v99
	v_cvt_f32_f16_sdwa v199, v99 dst_sel:DWORD dst_unused:UNUSED_PAD src0_sel:WORD_1
	v_cvt_f32_f16_e32 v200, v100
	v_cvt_f32_f16_sdwa v201, v100 dst_sel:DWORD dst_unused:UNUSED_PAD src0_sel:WORD_1
	v_cvt_f32_f16_e32 v202, v101
	v_cvt_f32_f16_sdwa v203, v101 dst_sel:DWORD dst_unused:UNUSED_PAD src0_sel:WORD_1
	v_pk_mul_f32 v[182:183], v[28:29], v[182:183]
	v_pk_mul_f32 v[184:185], v[30:31], v[184:185]
	v_pk_mul_f32 v[186:187], v[24:25], v[186:187]
	v_pk_mul_f32 v[188:189], v[26:27], v[188:189]
	v_pk_add_f32 v[182:183], v[182:183], v[196:197]
	v_pk_add_f32 v[184:185], v[184:185], v[198:199]
	v_pk_add_f32 v[186:187], v[186:187], v[200:201]
	v_pk_add_f32 v[188:189], v[188:189], v[202:203]
	v_cvt_pk_f16_f32 v28, v182, v183
	v_cvt_pk_f16_f32 v29, v184, v185
	v_cvt_pk_f16_f32 v30, v186, v187
	v_cvt_pk_f16_f32 v31, v188, v189
	global_store_dwordx4 v[236:237], v[28:31], off offset:256
	s_waitcnt vmcnt(10)
; __device__ __forceinline__ unsigned cvt_pk_f16(float lo, float hi) { f32x2 v = {lo, hi}; h16x2 b = __builtin_convertvector(v, h16x2); return __builtin_bit_cast(unsigned, b); }
;     __device__ __forceinline__ void operator()(const f32x4 (&acc)[2][2][4][2], const Unit& u, int wr, int wc, int fr, int fq) const {
;     ...
;         } else {
; #pragma unroll
;             for (int ai = 0; ai < 2; ++ai)
; #pragma unroll
;                 for (int mp = 0; mp < 2; ++mp) {
;                     h16x8 gv[2][2], pv[2][2];
; #pragma unroll
;                     for (int mm = 0; mm < 2; ++mm)
; #pragma unroll
;                         for (int bj = 0; bj < 2; ++bj) { const size_t row = (size_t)(row0 + ai * HALF + (2 * mp + mm) * 16);
;                             gv[mm][bj] = *(const h16x8*)(Gn + row * ldg + bj * HALF);
;                             if (n > 0) pv[mm][bj] = *(const h16x8*)(Mg + row * 1024 + col0 + bj * HALF); }
; #pragma unroll
;                     for (int mm = 0; mm < 2; ++mm)
; #pragma unroll
;                         for (int bj = 0; bj < 2; ++bj) { const int m = 2 * mp + mm; const size_t row = (size_t)(row0 + ai * HALF + m * 16);
;                             float o[8];
; #pragma unroll
;                             for (int e = 0; e < 8; ++e) { const float a = e < 4 ? acc[ai][bj][m][0][e] : acc[ai][bj][m][1][e - 4]; o[e] = a * (float)gv[mm][bj][e]; }
;                             if (n > 0) {
; #pragma unroll
;                                 for (int e = 0; e < 8; ++e) o[e] += (float)pv[mm][bj][e]; }
;                             u32x4 w; w.x = cvt_pk_f16(o[0], o[1]); w.y = cvt_pk_f16(o[2], o[3]); w.z = cvt_pk_f16(o[4], o[5]); w.w = cvt_pk_f16(o[6], o[7]);
;                             *(u32x4*)(Mg + row * 1024 + col0 + bj * HALF) = w; }
;                 }
;         }
	v_add_u32_e32 v238, 160, v176
	v_lshlrev_b32_e32 v240, 11, v238
	v_lshl_add_u64 v[236:237], v[180:181], 0, v[240:241]
	v_cvt_f32_f16_e32 v182, v130
	v_cvt_f32_f16_sdwa v183, v130 dst_sel:DWORD dst_unused:UNUSED_PAD src0_sel:WORD_1
	v_cvt_f32_f16_e32 v184, v131
	v_cvt_f32_f16_sdwa v185, v131 dst_sel:DWORD dst_unused:UNUSED_PAD src0_sel:WORD_1
	v_cvt_f32_f16_e32 v186, v132
	v_cvt_f32_f16_sdwa v187, v132 dst_sel:DWORD dst_unused:UNUSED_PAD src0_sel:WORD_1
	v_cvt_f32_f16_e32 v188, v133
	v_cvt_f32_f16_sdwa v189, v133 dst_sel:DWORD dst_unused:UNUSED_PAD src0_sel:WORD_1
	v_cvt_f32_f16_e32 v196, v138
	v_cvt_f32_f16_sdwa v197, v138 dst_sel:DWORD dst_unused:UNUSED_PAD src0_sel:WORD_1
	v_cvt_f32_f16_e32 v198, v139
	v_cvt_f32_f16_sdwa v199, v139 dst_sel:DWORD dst_unused:UNUSED_PAD src0_sel:WORD_1
	v_cvt_f32_f16_e32 v200, v140
	v_cvt_f32_f16_sdwa v201, v140 dst_sel:DWORD dst_unused:UNUSED_PAD src0_sel:WORD_1
	v_cvt_f32_f16_e32 v202, v141
	v_cvt_f32_f16_sdwa v203, v141 dst_sel:DWORD dst_unused:UNUSED_PAD src0_sel:WORD_1
	v_pk_mul_f32 v[182:183], v[20:21], v[182:183]
	v_pk_mul_f32 v[184:185], v[22:23], v[184:185]
	v_pk_mul_f32 v[186:187], v[16:17], v[186:187]
	v_pk_mul_f32 v[188:189], v[18:19], v[188:189]
	v_pk_add_f32 v[182:183], v[182:183], v[196:197]
	v_pk_add_f32 v[184:185], v[184:185], v[198:199]
	v_pk_add_f32 v[186:187], v[186:187], v[200:201]
	v_pk_add_f32 v[188:189], v[188:189], v[202:203]
	v_cvt_pk_f16_f32 v20, v182, v183
	v_cvt_pk_f16_f32 v21, v184, v185
	v_cvt_pk_f16_f32 v22, v186, v187
	v_cvt_pk_f16_f32 v23, v188, v189
	global_store_dwordx4 v[236:237], v[20:23], off
	v_cvt_f32_f16_e32 v182, v134
	v_cvt_f32_f16_sdwa v183, v134 dst_sel:DWORD dst_unused:UNUSED_PAD src0_sel:WORD_1
	v_cvt_f32_f16_e32 v184, v135
	v_cvt_f32_f16_sdwa v185, v135 dst_sel:DWORD dst_unused:UNUSED_PAD src0_sel:WORD_1
	v_cvt_f32_f16_e32 v186, v136
	v_cvt_f32_f16_sdwa v187, v136 dst_sel:DWORD dst_unused:UNUSED_PAD src0_sel:WORD_1
	v_cvt_f32_f16_e32 v188, v137
	v_cvt_f32_f16_sdwa v189, v137 dst_sel:DWORD dst_unused:UNUSED_PAD src0_sel:WORD_1
	v_cvt_f32_f16_e32 v196, v142
	v_cvt_f32_f16_sdwa v197, v142 dst_sel:DWORD dst_unused:UNUSED_PAD src0_sel:WORD_1
	v_cvt_f32_f16_e32 v198, v143
	v_cvt_f32_f16_sdwa v199, v143 dst_sel:DWORD dst_unused:UNUSED_PAD src0_sel:WORD_1
	v_cvt_f32_f16_e32 v200, v144
	v_cvt_f32_f16_sdwa v201, v144 dst_sel:DWORD dst_unused:UNUSED_PAD src0_sel:WORD_1
	v_cvt_f32_f16_e32 v202, v145
	v_cvt_f32_f16_sdwa v203, v145 dst_sel:DWORD dst_unused:UNUSED_PAD src0_sel:WORD_1
	v_pk_mul_f32 v[182:183], v[32:33], v[182:183]
	v_pk_mul_f32 v[184:185], v[34:35], v[184:185]
	v_pk_mul_f32 v[186:187], v[36:37], v[186:187]
	v_pk_mul_f32 v[188:189], v[38:39], v[188:189]
	v_pk_add_f32 v[182:183], v[182:183], v[196:197]
	v_pk_add_f32 v[184:185], v[184:185], v[198:199]
	v_pk_add_f32 v[186:187], v[186:187], v[200:201]
	v_pk_add_f32 v[188:189], v[188:189], v[202:203]
	v_cvt_pk_f16_f32 v32, v182, v183
	v_cvt_pk_f16_f32 v33, v184, v185
	v_cvt_pk_f16_f32 v34, v186, v187
	v_cvt_pk_f16_f32 v35, v188, v189
	global_store_dwordx4 v[236:237], v[32:35], off offset:256
	s_waitcnt vmcnt(8)
	v_add_u32_e32 v238, 176, v176
	v_lshlrev_b32_e32 v240, 11, v238
	v_lshl_add_u64 v[236:237], v[180:181], 0, v[240:241]
	v_cvt_f32_f16_e32 v182, v92
	v_cvt_f32_f16_sdwa v183, v92 dst_sel:DWORD dst_unused:UNUSED_PAD src0_sel:WORD_1
	v_cvt_f32_f16_e32 v184, v93
	v_cvt_f32_f16_sdwa v185, v93 dst_sel:DWORD dst_unused:UNUSED_PAD src0_sel:WORD_1
	v_cvt_f32_f16_e32 v186, v94
	v_cvt_f32_f16_sdwa v187, v94 dst_sel:DWORD dst_unused:UNUSED_PAD src0_sel:WORD_1
	v_cvt_f32_f16_e32 v188, v95
	v_cvt_f32_f16_sdwa v189, v95 dst_sel:DWORD dst_unused:UNUSED_PAD src0_sel:WORD_1
	v_cvt_f32_f16_e32 v196, v84
	v_cvt_f32_f16_sdwa v197, v84 dst_sel:DWORD dst_unused:UNUSED_PAD src0_sel:WORD_1
	v_cvt_f32_f16_e32 v198, v85
	v_cvt_f32_f16_sdwa v199, v85 dst_sel:DWORD dst_unused:UNUSED_PAD src0_sel:WORD_1
	v_cvt_f32_f16_e32 v200, v86
	v_cvt_f32_f16_sdwa v201, v86 dst_sel:DWORD dst_unused:UNUSED_PAD src0_sel:WORD_1
	v_cvt_f32_f16_e32 v202, v87
	v_cvt_f32_f16_sdwa v203, v87 dst_sel:DWORD dst_unused:UNUSED_PAD src0_sel:WORD_1
	v_pk_mul_f32 v[182:183], v[4:5], v[182:183]
	v_pk_mul_f32 v[184:185], v[6:7], v[184:185]
	v_pk_mul_f32 v[186:187], v[0:1], v[186:187]
	v_pk_mul_f32 v[188:189], v[2:3], v[188:189]
	v_pk_add_f32 v[182:183], v[182:183], v[196:197]
	v_pk_add_f32 v[184:185], v[184:185], v[198:199]
	v_pk_add_f32 v[186:187], v[186:187], v[200:201]
	v_pk_add_f32 v[188:189], v[188:189], v[202:203]
	v_cvt_pk_f16_f32 v4, v182, v183
	v_cvt_pk_f16_f32 v5, v184, v185
	v_cvt_pk_f16_f32 v6, v186, v187
	v_cvt_pk_f16_f32 v7, v188, v189
	global_store_dwordx4 v[236:237], v[4:7], off
	v_cvt_f32_f16_e32 v182, v88
	v_cvt_f32_f16_sdwa v183, v88 dst_sel:DWORD dst_unused:UNUSED_PAD src0_sel:WORD_1
	v_cvt_f32_f16_e32 v184, v89
	v_cvt_f32_f16_sdwa v185, v89 dst_sel:DWORD dst_unused:UNUSED_PAD src0_sel:WORD_1
	v_cvt_f32_f16_e32 v186, v90
	v_cvt_f32_f16_sdwa v187, v90 dst_sel:DWORD dst_unused:UNUSED_PAD src0_sel:WORD_1
	v_cvt_f32_f16_e32 v188, v91
	v_cvt_f32_f16_sdwa v189, v91 dst_sel:DWORD dst_unused:UNUSED_PAD src0_sel:WORD_1
	v_cvt_f32_f16_e32 v196, v80
	v_cvt_f32_f16_sdwa v197, v80 dst_sel:DWORD dst_unused:UNUSED_PAD src0_sel:WORD_1
	v_cvt_f32_f16_e32 v198, v81
	v_cvt_f32_f16_sdwa v199, v81 dst_sel:DWORD dst_unused:UNUSED_PAD src0_sel:WORD_1
	v_cvt_f32_f16_e32 v200, v82
	v_cvt_f32_f16_sdwa v201, v82 dst_sel:DWORD dst_unused:UNUSED_PAD src0_sel:WORD_1
	v_cvt_f32_f16_e32 v202, v83
	v_cvt_f32_f16_sdwa v203, v83 dst_sel:DWORD dst_unused:UNUSED_PAD src0_sel:WORD_1
	v_pk_mul_f32 v[182:183], v[8:9], v[182:183]
	v_pk_mul_f32 v[184:185], v[10:11], v[184:185]
	v_pk_mul_f32 v[186:187], v[12:13], v[186:187]
	v_pk_mul_f32 v[188:189], v[14:15], v[188:189]
	v_pk_add_f32 v[182:183], v[182:183], v[196:197]
	v_pk_add_f32 v[184:185], v[184:185], v[198:199]
	v_pk_add_f32 v[186:187], v[186:187], v[200:201]
	v_pk_add_f32 v[188:189], v[188:189], v[202:203]
	v_cvt_pk_f16_f32 v8, v182, v183
	v_cvt_pk_f16_f32 v9, v184, v185
	v_cvt_pk_f16_f32 v10, v186, v187
	v_cvt_pk_f16_f32 v11, v188, v189
	global_store_dwordx4 v[236:237], v[8:11], off offset:256
	s_branch .Lbrepi_done
; __device__ __forceinline__ unsigned cvt_pk_f16(float lo, float hi) { f32x2 v = {lo, hi}; h16x2 b = __builtin_convertvector(v, h16x2); return __builtin_bit_cast(unsigned, b); }
;     __device__ __forceinline__ void operator()(const f32x4 (&acc)[2][2][4][2], const Unit& u, int wr, int wc, int fr, int fq) const {
;     ...
;         } else {
; #pragma unroll
;             for (int ai = 0; ai < 2; ++ai)
; #pragma unroll
;                 for (int mp = 0; mp < 2; ++mp) {
;                     h16x8 gv[2][2], pv[2][2];
; #pragma unroll
;                     for (int mm = 0; mm < 2; ++mm)
; #pragma unroll
;                         for (int bj = 0; bj < 2; ++bj) { const size_t row = (size_t)(row0 + ai * HALF + (2 * mp + mm) * 16);
;                             gv[mm][bj] = *(const h16x8*)(Gn + row * ldg + bj * HALF);
;                             if (n > 0) pv[mm][bj] = *(const h16x8*)(Mg + row * 1024 + col0 + bj * HALF); }
; #pragma unroll
;                     for (int mm = 0; mm < 2; ++mm)
; #pragma unroll
;                         for (int bj = 0; bj < 2; ++bj) { const int m = 2 * mp + mm; const size_t row = (size_t)(row0 + ai * HALF + m * 16);
;                             float o[8];
; #pragma unroll
;                             for (int e = 0; e < 8; ++e) { const float a = e < 4 ? acc[ai][bj][m][0][e] : acc[ai][bj][m][1][e - 4]; o[e] = a * (float)gv[mm][bj][e]; }
;                             if (n > 0) {
; #pragma unroll
;                                 for (int e = 0; e < 8; ++e) o[e] += (float)pv[mm][bj][e]; }
;                             u32x4 w; w.x = cvt_pk_f16(o[0], o[1]); w.y = cvt_pk_f16(o[2], o[3]); w.z = cvt_pk_f16(o[4], o[5]); w.w = cvt_pk_f16(o[6], o[7]);
;                             *(u32x4*)(Mg + row * 1024 + col0 + bj * HALF) = w; }
;                 }
;         }
.Lbrepi_n2:
	v_readlane_b32 s40, v254, 46
	v_readlane_b32 s41, v254, 47
	v_mov_b32_e32 v241, 0
	s_nop 1
	v_lshl_add_u64 v[180:181], v[178:179], 1, s[40:41]
	v_mov_b32_e32 v238, v176
	v_mad_i64_i32 v[234:235], s[0:1], v238, s91, v[174:175]
	v_lshlrev_b32_e32 v240, 11, v238
	v_lshl_add_u64 v[236:237], v[180:181], 0, v[240:241]
	global_load_dwordx4 v[130:133], v[234:235], off
	global_load_dwordx4 v[138:141], v[236:237], off
	global_load_dwordx4 v[134:137], v[234:235], off offset:256
	global_load_dwordx4 v[142:145], v[236:237], off offset:256
	v_add_u32_e32 v238, 16, v176
	v_mad_i64_i32 v[234:235], s[0:1], v238, s91, v[174:175]
	v_lshlrev_b32_e32 v240, 11, v238
	v_lshl_add_u64 v[236:237], v[180:181], 0, v[240:241]
	global_load_dwordx4 v[146:149], v[234:235], off
	global_load_dwordx4 v[154:157], v[236:237], off
	global_load_dwordx4 v[150:153], v[234:235], off offset:256
	global_load_dwordx4 v[158:161], v[236:237], off offset:256
	s_waitcnt vmcnt(4)
	v_mov_b32_e32 v238, v176
	v_lshlrev_b32_e32 v240, 11, v238
	v_lshl_add_u64 v[236:237], v[180:181], 0, v[240:241]
	v_cvt_f32_f16_e32 v182, v130
	v_cvt_f32_f16_sdwa v183, v130 dst_sel:DWORD dst_unused:UNUSED_PAD src0_sel:WORD_1
	v_cvt_f32_f16_e32 v184, v131
	v_cvt_f32_f16_sdwa v185, v131 dst_sel:DWORD dst_unused:UNUSED_PAD src0_sel:WORD_1
	v_cvt_f32_f16_e32 v186, v132
	v_cvt_f32_f16_sdwa v187, v132 dst_sel:DWORD dst_unused:UNUSED_PAD src0_sel:WORD_1
	v_cvt_f32_f16_e32 v188, v133
	v_cvt_f32_f16_sdwa v189, v133 dst_sel:DWORD dst_unused:UNUSED_PAD src0_sel:WORD_1
	v_cvt_f32_f16_e32 v196, v138
	v_cvt_f32_f16_sdwa v197, v138 dst_sel:DWORD dst_unused:UNUSED_PAD src0_sel:WORD_1
	v_cvt_f32_f16_e32 v198, v139
	v_cvt_f32_f16_sdwa v199, v139 dst_sel:DWORD dst_unused:UNUSED_PAD src0_sel:WORD_1
	v_cvt_f32_f16_e32 v200, v140
	v_cvt_f32_f16_sdwa v201, v140 dst_sel:DWORD dst_unused:UNUSED_PAD src0_sel:WORD_1
	v_cvt_f32_f16_e32 v202, v141
	v_cvt_f32_f16_sdwa v203, v141 dst_sel:DWORD dst_unused:UNUSED_PAD src0_sel:WORD_1
	v_pk_mul_f32 v[182:183], v[126:127], v[182:183]
	v_pk_mul_f32 v[184:185], v[128:129], v[184:185]
	v_pk_mul_f32 v[186:187], v[122:123], v[186:187]
	v_pk_mul_f32 v[188:189], v[124:125], v[188:189]
	v_pk_add_f32 v[182:183], v[182:183], v[196:197]
	v_pk_add_f32 v[184:185], v[184:185], v[198:199]
	v_pk_add_f32 v[186:187], v[186:187], v[200:201]
	v_pk_add_f32 v[188:189], v[188:189], v[202:203]
	v_cvt_pk_f16_f32 v126, v182, v183
	v_cvt_pk_f16_f32 v127, v184, v185
	v_cvt_pk_f16_f32 v128, v186, v187
	v_cvt_pk_f16_f32 v129, v188, v189
	global_store_dwordx4 v[236:237], v[126:129], off sc1
	v_cvt_f32_f16_e32 v182, v134
	v_cvt_f32_f16_sdwa v183, v134 dst_sel:DWORD dst_unused:UNUSED_PAD src0_sel:WORD_1
	v_cvt_f32_f16_e32 v184, v135
	v_cvt_f32_f16_sdwa v185, v135 dst_sel:DWORD dst_unused:UNUSED_PAD src0_sel:WORD_1
	v_cvt_f32_f16_e32 v186, v136
	v_cvt_f32_f16_sdwa v187, v136 dst_sel:DWORD dst_unused:UNUSED_PAD src0_sel:WORD_1
	v_cvt_f32_f16_e32 v188, v137
	v_cvt_f32_f16_sdwa v189, v137 dst_sel:DWORD dst_unused:UNUSED_PAD src0_sel:WORD_1
	v_cvt_f32_f16_e32 v196, v142
	v_cvt_f32_f16_sdwa v197, v142 dst_sel:DWORD dst_unused:UNUSED_PAD src0_sel:WORD_1
	v_cvt_f32_f16_e32 v198, v143
	v_cvt_f32_f16_sdwa v199, v143 dst_sel:DWORD dst_unused:UNUSED_PAD src0_sel:WORD_1
	v_cvt_f32_f16_e32 v200, v144
	v_cvt_f32_f16_sdwa v201, v144 dst_sel:DWORD dst_unused:UNUSED_PAD src0_sel:WORD_1
	v_cvt_f32_f16_e32 v202, v145
	v_cvt_f32_f16_sdwa v203, v145 dst_sel:DWORD dst_unused:UNUSED_PAD src0_sel:WORD_1
	v_pk_mul_f32 v[182:183], v[118:119], v[182:183]
	v_pk_mul_f32 v[184:185], v[120:121], v[184:185]
	v_pk_mul_f32 v[186:187], v[114:115], v[186:187]
	v_pk_mul_f32 v[188:189], v[116:117], v[188:189]
	v_pk_add_f32 v[182:183], v[182:183], v[196:197]
	v_pk_add_f32 v[184:185], v[184:185], v[198:199]
	v_pk_add_f32 v[186:187], v[186:187], v[200:201]
	v_pk_add_f32 v[188:189], v[188:189], v[202:203]
	v_cvt_pk_f16_f32 v118, v182, v183
	v_cvt_pk_f16_f32 v119, v184, v185
	v_cvt_pk_f16_f32 v120, v186, v187
	v_cvt_pk_f16_f32 v121, v188, v189
	global_store_dwordx4 v[236:237], v[118:121], off offset:256 sc1
	v_add_u32_e32 v238, 32, v176
	v_mad_i64_i32 v[234:235], s[0:1], v238, s91, v[174:175]
	v_lshlrev_b32_e32 v240, 11, v238
	v_lshl_add_u64 v[236:237], v[180:181], 0, v[240:241]
	global_load_dwordx4 v[130:133], v[234:235], off
	global_load_dwordx4 v[138:141], v[236:237], off
	global_load_dwordx4 v[134:137], v[234:235], off offset:256
	global_load_dwordx4 v[142:145], v[236:237], off offset:256
	s_nop 1
	v_add_u32_e32 v238, 48, v176
	v_mad_i64_i32 v[234:235], s[0:1], v238, s91, v[174:175]
	v_lshlrev_b32_e32 v240, 11, v238
	v_lshl_add_u64 v[236:237], v[180:181], 0, v[240:241]
	global_load_dwordx4 v[126:129], v[234:235], off
	global_load_dwordx4 v[118:121], v[236:237], off
	global_load_dwordx4 v[122:125], v[234:235], off offset:256
	global_load_dwordx4 v[114:117], v[236:237], off offset:256
	s_waitcnt vmcnt(10)
; __device__ __forceinline__ unsigned cvt_pk_f16(float lo, float hi) { f32x2 v = {lo, hi}; h16x2 b = __builtin_convertvector(v, h16x2); return __builtin_bit_cast(unsigned, b); }
;     __device__ __forceinline__ void operator()(const f32x4 (&acc)[2][2][4][2], const Unit& u, int wr, int wc, int fr, int fq) const {
;     ...
;                 for (int mp = 0; mp < 2; ++mp) {
;                     h16x8 gv[2][2], pv[2][2];
; #pragma unroll
;                     for (int mm = 0; mm < 2; ++mm)
; #pragma unroll
;                         for (int bj = 0; bj < 2; ++bj) { const size_t row = (size_t)(row0 + ai * HALF + (2 * mp + mm) * 16);
;                             gv[mm][bj] = *(const h16x8*)(Gn + row * ldg + bj * HALF);
;                             if (n > 0) pv[mm][bj] = *(const h16x8*)(Mg + row * 1024 + col0 + bj * HALF); }
; #pragma unroll
;                     for (int mm = 0; mm < 2; ++mm)
; #pragma unroll
;                         for (int bj = 0; bj < 2; ++bj) { const int m = 2 * mp + mm; const size_t row = (size_t)(row0 + ai * HALF + m * 16);
;                             float o[8];
; #pragma unroll
;                             for (int e = 0; e < 8; ++e) { const float a = e < 4 ? acc[ai][bj][m][0][e] : acc[ai][bj][m][1][e - 4]; o[e] = a * (float)gv[mm][bj][e]; }
;                             if (n > 0) {
; #pragma unroll
;                                 for (int e = 0; e < 8; ++e) o[e] += (float)pv[mm][bj][e]; }
;                             u32x4 w; w.x = cvt_pk_f16(o[0], o[1]); w.y = cvt_pk_f16(o[2], o[3]); w.z = cvt_pk_f16(o[4], o[5]); w.w = cvt_pk_f16(o[6], o[7]);
;                             *(u32x4*)(Mg + row * 1024 + col0 + bj * HALF) = w; }
	v_add_u32_e32 v238, 16, v176
	v_lshlrev_b32_e32 v240, 11, v238
	v_lshl_add_u64 v[236:237], v[180:181], 0, v[240:241]
	v_cvt_f32_f16_e32 v182, v146
	v_cvt_f32_f16_sdwa v183, v146 dst_sel:DWORD dst_unused:UNUSED_PAD src0_sel:WORD_1
	v_cvt_f32_f16_e32 v184, v147
	v_cvt_f32_f16_sdwa v185, v147 dst_sel:DWORD dst_unused:UNUSED_PAD src0_sel:WORD_1
	v_cvt_f32_f16_e32 v186, v148
	v_cvt_f32_f16_sdwa v187, v148 dst_sel:DWORD dst_unused:UNUSED_PAD src0_sel:WORD_1
	v_cvt_f32_f16_e32 v188, v149
	v_cvt_f32_f16_sdwa v189, v149 dst_sel:DWORD dst_unused:UNUSED_PAD src0_sel:WORD_1
	v_cvt_f32_f16_e32 v196, v154
	v_cvt_f32_f16_sdwa v197, v154 dst_sel:DWORD dst_unused:UNUSED_PAD src0_sel:WORD_1
	v_cvt_f32_f16_e32 v198, v155
	v_cvt_f32_f16_sdwa v199, v155 dst_sel:DWORD dst_unused:UNUSED_PAD src0_sel:WORD_1
	v_cvt_f32_f16_e32 v200, v156
	v_cvt_f32_f16_sdwa v201, v156 dst_sel:DWORD dst_unused:UNUSED_PAD src0_sel:WORD_1
	v_cvt_f32_f16_e32 v202, v157
	v_cvt_f32_f16_sdwa v203, v157 dst_sel:DWORD dst_unused:UNUSED_PAD src0_sel:WORD_1
	v_pk_mul_f32 v[182:183], v[110:111], v[182:183]
	v_pk_mul_f32 v[184:185], v[112:113], v[184:185]
	v_pk_mul_f32 v[186:187], v[106:107], v[186:187]
	v_pk_mul_f32 v[188:189], v[108:109], v[188:189]
	v_pk_add_f32 v[182:183], v[182:183], v[196:197]
	v_pk_add_f32 v[184:185], v[184:185], v[198:199]
	v_pk_add_f32 v[186:187], v[186:187], v[200:201]
	v_pk_add_f32 v[188:189], v[188:189], v[202:203]
	v_cvt_pk_f16_f32 v110, v182, v183
	v_cvt_pk_f16_f32 v111, v184, v185
	v_cvt_pk_f16_f32 v112, v186, v187
	v_cvt_pk_f16_f32 v113, v188, v189
	global_store_dwordx4 v[236:237], v[110:113], off sc1
	v_cvt_f32_f16_e32 v182, v150
	v_cvt_f32_f16_sdwa v183, v150 dst_sel:DWORD dst_unused:UNUSED_PAD src0_sel:WORD_1
	v_cvt_f32_f16_e32 v184, v151
	v_cvt_f32_f16_sdwa v185, v151 dst_sel:DWORD dst_unused:UNUSED_PAD src0_sel:WORD_1
	v_cvt_f32_f16_e32 v186, v152
	v_cvt_f32_f16_sdwa v187, v152 dst_sel:DWORD dst_unused:UNUSED_PAD src0_sel:WORD_1
	v_cvt_f32_f16_e32 v188, v153
	v_cvt_f32_f16_sdwa v189, v153 dst_sel:DWORD dst_unused:UNUSED_PAD src0_sel:WORD_1
	v_cvt_f32_f16_e32 v196, v158
	v_cvt_f32_f16_sdwa v197, v158 dst_sel:DWORD dst_unused:UNUSED_PAD src0_sel:WORD_1
	v_cvt_f32_f16_e32 v198, v159
	v_cvt_f32_f16_sdwa v199, v159 dst_sel:DWORD dst_unused:UNUSED_PAD src0_sel:WORD_1
	v_cvt_f32_f16_e32 v200, v160
	v_cvt_f32_f16_sdwa v201, v160 dst_sel:DWORD dst_unused:UNUSED_PAD src0_sel:WORD_1
	v_cvt_f32_f16_e32 v202, v161
	v_cvt_f32_f16_sdwa v203, v161 dst_sel:DWORD dst_unused:UNUSED_PAD src0_sel:WORD_1
	v_pk_mul_f32 v[182:183], v[102:103], v[182:183]
	v_pk_mul_f32 v[184:185], v[104:105], v[184:185]
	v_pk_mul_f32 v[186:187], v[98:99], v[186:187]
	v_pk_mul_f32 v[188:189], v[100:101], v[188:189]
	v_pk_add_f32 v[182:183], v[182:183], v[196:197]
	v_pk_add_f32 v[184:185], v[184:185], v[198:199]
	v_pk_add_f32 v[186:187], v[186:187], v[200:201]
	v_pk_add_f32 v[188:189], v[188:189], v[202:203]
	v_cvt_pk_f16_f32 v102, v182, v183
	v_cvt_pk_f16_f32 v103, v184, v185
	v_cvt_pk_f16_f32 v104, v186, v187
	v_cvt_pk_f16_f32 v105, v188, v189
	global_store_dwordx4 v[236:237], v[102:105], off offset:256 sc1
	v_add_u32_e32 v238, 128, v176
	v_mad_i64_i32 v[234:235], s[0:1], v238, s91, v[174:175]
	v_lshlrev_b32_e32 v240, 11, v238
	v_lshl_add_u64 v[236:237], v[180:181], 0, v[240:241]
	global_load_dwordx4 v[146:149], v[234:235], off
	global_load_dwordx4 v[154:157], v[236:237], off
	global_load_dwordx4 v[150:153], v[234:235], off offset:256
	global_load_dwordx4 v[158:161], v[236:237], off offset:256
	s_nop 1
	v_add_u32_e32 v238, 144, v176
	v_mad_i64_i32 v[234:235], s[0:1], v238, s91, v[174:175]
	v_lshlrev_b32_e32 v240, 11, v238
	v_lshl_add_u64 v[236:237], v[180:181], 0, v[240:241]
	global_load_dwordx4 v[110:113], v[234:235], off
	global_load_dwordx4 v[102:105], v[236:237], off
	global_load_dwordx4 v[106:109], v[234:235], off offset:256
	global_load_dwordx4 v[98:101], v[236:237], off offset:256
	s_waitcnt vmcnt(14)
	v_add_u32_e32 v238, 32, v176
	v_lshlrev_b32_e32 v240, 11, v238
	v_lshl_add_u64 v[236:237], v[180:181], 0, v[240:241]
	v_cvt_f32_f16_e32 v182, v130
	v_cvt_f32_f16_sdwa v183, v130 dst_sel:DWORD dst_unused:UNUSED_PAD src0_sel:WORD_1
	v_cvt_f32_f16_e32 v184, v131
	v_cvt_f32_f16_sdwa v185, v131 dst_sel:DWORD dst_unused:UNUSED_PAD src0_sel:WORD_1
	v_cvt_f32_f16_e32 v186, v132
	v_cvt_f32_f16_sdwa v187, v132 dst_sel:DWORD dst_unused:UNUSED_PAD src0_sel:WORD_1
	v_cvt_f32_f16_e32 v188, v133
	v_cvt_f32_f16_sdwa v189, v133 dst_sel:DWORD dst_unused:UNUSED_PAD src0_sel:WORD_1
	v_cvt_f32_f16_e32 v196, v138
	v_cvt_f32_f16_sdwa v197, v138 dst_sel:DWORD dst_unused:UNUSED_PAD src0_sel:WORD_1
	v_cvt_f32_f16_e32 v198, v139
	v_cvt_f32_f16_sdwa v199, v139 dst_sel:DWORD dst_unused:UNUSED_PAD src0_sel:WORD_1
	v_cvt_f32_f16_e32 v200, v140
	v_cvt_f32_f16_sdwa v201, v140 dst_sel:DWORD dst_unused:UNUSED_PAD src0_sel:WORD_1
	v_cvt_f32_f16_e32 v202, v141
	v_cvt_f32_f16_sdwa v203, v141 dst_sel:DWORD dst_unused:UNUSED_PAD src0_sel:WORD_1
	v_pk_mul_f32 v[182:183], v[92:93], v[182:183]
	v_pk_mul_f32 v[184:185], v[94:95], v[184:185]
	v_pk_mul_f32 v[186:187], v[88:89], v[186:187]
	v_pk_mul_f32 v[188:189], v[90:91], v[188:189]
	v_pk_add_f32 v[182:183], v[182:183], v[196:197]
	v_pk_add_f32 v[184:185], v[184:185], v[198:199]
	v_pk_add_f32 v[186:187], v[186:187], v[200:201]
	v_pk_add_f32 v[188:189], v[188:189], v[202:203]
	v_cvt_pk_f16_f32 v92, v182, v183
	v_cvt_pk_f16_f32 v93, v184, v185
	v_cvt_pk_f16_f32 v94, v186, v187
	v_cvt_pk_f16_f32 v95, v188, v189
	global_store_dwordx4 v[236:237], v[92:95], off sc1
	v_cvt_f32_f16_e32 v182, v134
	v_cvt_f32_f16_sdwa v183, v134 dst_sel:DWORD dst_unused:UNUSED_PAD src0_sel:WORD_1
; __device__ __forceinline__ unsigned cvt_pk_f16(float lo, float hi) { f32x2 v = {lo, hi}; h16x2 b = __builtin_convertvector(v, h16x2); return __builtin_bit_cast(unsigned, b); }
;     __device__ __forceinline__ void operator()(const f32x4 (&acc)[2][2][4][2], const Unit& u, int wr, int wc, int fr, int fq) const {
;     ...
;                 for (int mp = 0; mp < 2; ++mp) {
;                     h16x8 gv[2][2], pv[2][2];
; #pragma unroll
;                     for (int mm = 0; mm < 2; ++mm)
; #pragma unroll
;                         for (int bj = 0; bj < 2; ++bj) { const size_t row = (size_t)(row0 + ai * HALF + (2 * mp + mm) * 16);
;                             gv[mm][bj] = *(const h16x8*)(Gn + row * ldg + bj * HALF);
;                             if (n > 0) pv[mm][bj] = *(const h16x8*)(Mg + row * 1024 + col0 + bj * HALF); }
; #pragma unroll
;                     for (int mm = 0; mm < 2; ++mm)
; #pragma unroll
;                         for (int bj = 0; bj < 2; ++bj) { const int m = 2 * mp + mm; const size_t row = (size_t)(row0 + ai * HALF + m * 16);
;                             float o[8];
; #pragma unroll
;                             for (int e = 0; e < 8; ++e) { const float a = e < 4 ? acc[ai][bj][m][0][e] : acc[ai][bj][m][1][e - 4]; o[e] = a * (float)gv[mm][bj][e]; }
;                             if (n > 0) {
; #pragma unroll
;                                 for (int e = 0; e < 8; ++e) o[e] += (float)pv[mm][bj][e]; }
;                             u32x4 w; w.x = cvt_pk_f16(o[0], o[1]); w.y = cvt_pk_f16(o[2], o[3]); w.z = cvt_pk_f16(o[4], o[5]); w.w = cvt_pk_f16(o[6], o[7]);
;                             *(u32x4*)(Mg + row * 1024 + col0 + bj * HALF) = w; }
	v_cvt_f32_f16_e32 v184, v135
	v_cvt_f32_f16_sdwa v185, v135 dst_sel:DWORD dst_unused:UNUSED_PAD src0_sel:WORD_1
	v_cvt_f32_f16_e32 v186, v136
	v_cvt_f32_f16_sdwa v187, v136 dst_sel:DWORD dst_unused:UNUSED_PAD src0_sel:WORD_1
	v_cvt_f32_f16_e32 v188, v137
	v_cvt_f32_f16_sdwa v189, v137 dst_sel:DWORD dst_unused:UNUSED_PAD src0_sel:WORD_1
	v_cvt_f32_f16_e32 v196, v142
	v_cvt_f32_f16_sdwa v197, v142 dst_sel:DWORD dst_unused:UNUSED_PAD src0_sel:WORD_1
	v_cvt_f32_f16_e32 v198, v143
	v_cvt_f32_f16_sdwa v199, v143 dst_sel:DWORD dst_unused:UNUSED_PAD src0_sel:WORD_1
	v_cvt_f32_f16_e32 v200, v144
	v_cvt_f32_f16_sdwa v201, v144 dst_sel:DWORD dst_unused:UNUSED_PAD src0_sel:WORD_1
	v_cvt_f32_f16_e32 v202, v145
	v_cvt_f32_f16_sdwa v203, v145 dst_sel:DWORD dst_unused:UNUSED_PAD src0_sel:WORD_1
	v_pk_mul_f32 v[182:183], v[84:85], v[182:183]
	v_pk_mul_f32 v[184:185], v[86:87], v[184:185]
	v_pk_mul_f32 v[186:187], v[80:81], v[186:187]
	v_pk_mul_f32 v[188:189], v[82:83], v[188:189]
	v_pk_add_f32 v[182:183], v[182:183], v[196:197]
	v_pk_add_f32 v[184:185], v[184:185], v[198:199]
	v_pk_add_f32 v[186:187], v[186:187], v[200:201]
	v_pk_add_f32 v[188:189], v[188:189], v[202:203]
	v_cvt_pk_f16_f32 v84, v182, v183
	v_cvt_pk_f16_f32 v85, v184, v185
	v_cvt_pk_f16_f32 v86, v186, v187
	v_cvt_pk_f16_f32 v87, v188, v189
	global_store_dwordx4 v[236:237], v[84:87], off offset:256 sc1
	v_add_u32_e32 v238, 160, v176
	v_mad_i64_i32 v[234:235], s[0:1], v238, s91, v[174:175]
	v_lshlrev_b32_e32 v240, 11, v238
	v_lshl_add_u64 v[236:237], v[180:181], 0, v[240:241]
	global_load_dwordx4 v[130:133], v[234:235], off
	global_load_dwordx4 v[138:141], v[236:237], off
	global_load_dwordx4 v[134:137], v[234:235], off offset:256
	global_load_dwordx4 v[142:145], v[236:237], off offset:256
	s_nop 1
	v_add_u32_e32 v238, 176, v176
	v_mad_i64_i32 v[234:235], s[0:1], v238, s91, v[174:175]
	v_lshlrev_b32_e32 v240, 11, v238
	v_lshl_add_u64 v[236:237], v[180:181], 0, v[240:241]
	global_load_dwordx4 v[92:95], v[234:235], off
	global_load_dwordx4 v[84:87], v[236:237], off
	global_load_dwordx4 v[88:91], v[234:235], off offset:256
	global_load_dwordx4 v[80:83], v[236:237], off offset:256
	s_waitcnt vmcnt(20)
	v_add_u32_e32 v238, 48, v176
	v_lshlrev_b32_e32 v240, 11, v238
	v_lshl_add_u64 v[236:237], v[180:181], 0, v[240:241]
	v_cvt_f32_f16_e32 v182, v126
	v_cvt_f32_f16_sdwa v183, v126 dst_sel:DWORD dst_unused:UNUSED_PAD src0_sel:WORD_1
	v_cvt_f32_f16_e32 v184, v127
	v_cvt_f32_f16_sdwa v185, v127 dst_sel:DWORD dst_unused:UNUSED_PAD src0_sel:WORD_1
	v_cvt_f32_f16_e32 v186, v128
	v_cvt_f32_f16_sdwa v187, v128 dst_sel:DWORD dst_unused:UNUSED_PAD src0_sel:WORD_1
	v_cvt_f32_f16_e32 v188, v129
	v_cvt_f32_f16_sdwa v189, v129 dst_sel:DWORD dst_unused:UNUSED_PAD src0_sel:WORD_1
	v_cvt_f32_f16_e32 v196, v118
	v_cvt_f32_f16_sdwa v197, v118 dst_sel:DWORD dst_unused:UNUSED_PAD src0_sel:WORD_1
	v_cvt_f32_f16_e32 v198, v119
	v_cvt_f32_f16_sdwa v199, v119 dst_sel:DWORD dst_unused:UNUSED_PAD src0_sel:WORD_1
	v_cvt_f32_f16_e32 v200, v120
	v_cvt_f32_f16_sdwa v201, v120 dst_sel:DWORD dst_unused:UNUSED_PAD src0_sel:WORD_1
	v_cvt_f32_f16_e32 v202, v121
	v_cvt_f32_f16_sdwa v203, v121 dst_sel:DWORD dst_unused:UNUSED_PAD src0_sel:WORD_1
	v_pk_mul_f32 v[182:183], v[76:77], v[182:183]
	v_pk_mul_f32 v[184:185], v[78:79], v[184:185]
	v_pk_mul_f32 v[186:187], v[72:73], v[186:187]
	v_pk_mul_f32 v[188:189], v[74:75], v[188:189]
	v_pk_add_f32 v[182:183], v[182:183], v[196:197]
	v_pk_add_f32 v[184:185], v[184:185], v[198:199]
	v_pk_add_f32 v[186:187], v[186:187], v[200:201]
	v_pk_add_f32 v[188:189], v[188:189], v[202:203]
	v_cvt_pk_f16_f32 v76, v182, v183
	v_cvt_pk_f16_f32 v77, v184, v185
	v_cvt_pk_f16_f32 v78, v186, v187
	v_cvt_pk_f16_f32 v79, v188, v189
	global_store_dwordx4 v[236:237], v[76:79], off sc1
	v_cvt_f32_f16_e32 v182, v122
	v_cvt_f32_f16_sdwa v183, v122 dst_sel:DWORD dst_unused:UNUSED_PAD src0_sel:WORD_1
	v_cvt_f32_f16_e32 v184, v123
	v_cvt_f32_f16_sdwa v185, v123 dst_sel:DWORD dst_unused:UNUSED_PAD src0_sel:WORD_1
	v_cvt_f32_f16_e32 v186, v124
	v_cvt_f32_f16_sdwa v187, v124 dst_sel:DWORD dst_unused:UNUSED_PAD src0_sel:WORD_1
	v_cvt_f32_f16_e32 v188, v125
	v_cvt_f32_f16_sdwa v189, v125 dst_sel:DWORD dst_unused:UNUSED_PAD src0_sel:WORD_1
	v_cvt_f32_f16_e32 v196, v114
	v_cvt_f32_f16_sdwa v197, v114 dst_sel:DWORD dst_unused:UNUSED_PAD src0_sel:WORD_1
	v_cvt_f32_f16_e32 v198, v115
	v_cvt_f32_f16_sdwa v199, v115 dst_sel:DWORD dst_unused:UNUSED_PAD src0_sel:WORD_1
	v_cvt_f32_f16_e32 v200, v116
	v_cvt_f32_f16_sdwa v201, v116 dst_sel:DWORD dst_unused:UNUSED_PAD src0_sel:WORD_1
	v_cvt_f32_f16_e32 v202, v117
	v_cvt_f32_f16_sdwa v203, v117 dst_sel:DWORD dst_unused:UNUSED_PAD src0_sel:WORD_1
	v_pk_mul_f32 v[182:183], v[68:69], v[182:183]
	v_pk_mul_f32 v[184:185], v[70:71], v[184:185]
	v_pk_mul_f32 v[186:187], v[64:65], v[186:187]
	v_pk_mul_f32 v[188:189], v[66:67], v[188:189]
	v_pk_add_f32 v[182:183], v[182:183], v[196:197]
	v_pk_add_f32 v[184:185], v[184:185], v[198:199]
	v_pk_add_f32 v[186:187], v[186:187], v[200:201]
	v_pk_add_f32 v[188:189], v[188:189], v[202:203]
	v_cvt_pk_f16_f32 v68, v182, v183
	v_cvt_pk_f16_f32 v69, v184, v185
	v_cvt_pk_f16_f32 v70, v186, v187
	v_cvt_pk_f16_f32 v71, v188, v189
	global_store_dwordx4 v[236:237], v[68:71], off offset:256 sc1
	s_waitcnt vmcnt(16)
; __device__ __forceinline__ unsigned cvt_pk_f16(float lo, float hi) { f32x2 v = {lo, hi}; h16x2 b = __builtin_convertvector(v, h16x2); return __builtin_bit_cast(unsigned, b); }
;     __device__ __forceinline__ void operator()(const f32x4 (&acc)[2][2][4][2], const Unit& u, int wr, int wc, int fr, int fq) const {
;     ...
;                 for (int mp = 0; mp < 2; ++mp) {
;                     h16x8 gv[2][2], pv[2][2];
; #pragma unroll
;                     for (int mm = 0; mm < 2; ++mm)
; #pragma unroll
;                         for (int bj = 0; bj < 2; ++bj) { const size_t row = (size_t)(row0 + ai * HALF + (2 * mp + mm) * 16);
;                             gv[mm][bj] = *(const h16x8*)(Gn + row * ldg + bj * HALF);
;                             if (n > 0) pv[mm][bj] = *(const h16x8*)(Mg + row * 1024 + col0 + bj * HALF); }
; #pragma unroll
;                     for (int mm = 0; mm < 2; ++mm)
; #pragma unroll
;                         for (int bj = 0; bj < 2; ++bj) { const int m = 2 * mp + mm; const size_t row = (size_t)(row0 + ai * HALF + m * 16);
;                             float o[8];
; #pragma unroll
;                             for (int e = 0; e < 8; ++e) { const float a = e < 4 ? acc[ai][bj][m][0][e] : acc[ai][bj][m][1][e - 4]; o[e] = a * (float)gv[mm][bj][e]; }
;                             if (n > 0) {
; #pragma unroll
;                                 for (int e = 0; e < 8; ++e) o[e] += (float)pv[mm][bj][e]; }
;                             u32x4 w; w.x = cvt_pk_f16(o[0], o[1]); w.y = cvt_pk_f16(o[2], o[3]); w.z = cvt_pk_f16(o[4], o[5]); w.w = cvt_pk_f16(o[6], o[7]);
;                             *(u32x4*)(Mg + row * 1024 + col0 + bj * HALF) = w; }
	v_add_u32_e32 v238, 128, v176
	v_lshlrev_b32_e32 v240, 11, v238
	v_lshl_add_u64 v[236:237], v[180:181], 0, v[240:241]
	v_cvt_f32_f16_e32 v182, v146
	v_cvt_f32_f16_sdwa v183, v146 dst_sel:DWORD dst_unused:UNUSED_PAD src0_sel:WORD_1
	v_cvt_f32_f16_e32 v184, v147
	v_cvt_f32_f16_sdwa v185, v147 dst_sel:DWORD dst_unused:UNUSED_PAD src0_sel:WORD_1
	v_cvt_f32_f16_e32 v186, v148
	v_cvt_f32_f16_sdwa v187, v148 dst_sel:DWORD dst_unused:UNUSED_PAD src0_sel:WORD_1
	v_cvt_f32_f16_e32 v188, v149
	v_cvt_f32_f16_sdwa v189, v149 dst_sel:DWORD dst_unused:UNUSED_PAD src0_sel:WORD_1
	v_cvt_f32_f16_e32 v196, v154
	v_cvt_f32_f16_sdwa v197, v154 dst_sel:DWORD dst_unused:UNUSED_PAD src0_sel:WORD_1
	v_cvt_f32_f16_e32 v198, v155
	v_cvt_f32_f16_sdwa v199, v155 dst_sel:DWORD dst_unused:UNUSED_PAD src0_sel:WORD_1
	v_cvt_f32_f16_e32 v200, v156
	v_cvt_f32_f16_sdwa v201, v156 dst_sel:DWORD dst_unused:UNUSED_PAD src0_sel:WORD_1
	v_cvt_f32_f16_e32 v202, v157
	v_cvt_f32_f16_sdwa v203, v157 dst_sel:DWORD dst_unused:UNUSED_PAD src0_sel:WORD_1
	v_pk_mul_f32 v[182:183], v[60:61], v[182:183]
	v_pk_mul_f32 v[184:185], v[62:63], v[184:185]
	v_pk_mul_f32 v[186:187], v[56:57], v[186:187]
	v_pk_mul_f32 v[188:189], v[58:59], v[188:189]
	v_pk_add_f32 v[182:183], v[182:183], v[196:197]
	v_pk_add_f32 v[184:185], v[184:185], v[198:199]
	v_pk_add_f32 v[186:187], v[186:187], v[200:201]
	v_pk_add_f32 v[188:189], v[188:189], v[202:203]
	v_cvt_pk_f16_f32 v60, v182, v183
	v_cvt_pk_f16_f32 v61, v184, v185
	v_cvt_pk_f16_f32 v62, v186, v187
	v_cvt_pk_f16_f32 v63, v188, v189
	global_store_dwordx4 v[236:237], v[60:63], off sc1
	v_cvt_f32_f16_e32 v182, v150
	v_cvt_f32_f16_sdwa v183, v150 dst_sel:DWORD dst_unused:UNUSED_PAD src0_sel:WORD_1
	v_cvt_f32_f16_e32 v184, v151
	v_cvt_f32_f16_sdwa v185, v151 dst_sel:DWORD dst_unused:UNUSED_PAD src0_sel:WORD_1
	v_cvt_f32_f16_e32 v186, v152
	v_cvt_f32_f16_sdwa v187, v152 dst_sel:DWORD dst_unused:UNUSED_PAD src0_sel:WORD_1
	v_cvt_f32_f16_e32 v188, v153
	v_cvt_f32_f16_sdwa v189, v153 dst_sel:DWORD dst_unused:UNUSED_PAD src0_sel:WORD_1
	v_cvt_f32_f16_e32 v196, v158
	v_cvt_f32_f16_sdwa v197, v158 dst_sel:DWORD dst_unused:UNUSED_PAD src0_sel:WORD_1
	v_cvt_f32_f16_e32 v198, v159
	v_cvt_f32_f16_sdwa v199, v159 dst_sel:DWORD dst_unused:UNUSED_PAD src0_sel:WORD_1
	v_cvt_f32_f16_e32 v200, v160
	v_cvt_f32_f16_sdwa v201, v160 dst_sel:DWORD dst_unused:UNUSED_PAD src0_sel:WORD_1
	v_cvt_f32_f16_e32 v202, v161
	v_cvt_f32_f16_sdwa v203, v161 dst_sel:DWORD dst_unused:UNUSED_PAD src0_sel:WORD_1
	v_pk_mul_f32 v[182:183], v[52:53], v[182:183]
	v_pk_mul_f32 v[184:185], v[54:55], v[184:185]
	v_pk_mul_f32 v[186:187], v[48:49], v[186:187]
	v_pk_mul_f32 v[188:189], v[50:51], v[188:189]
	v_pk_add_f32 v[182:183], v[182:183], v[196:197]
	v_pk_add_f32 v[184:185], v[184:185], v[198:199]
	v_pk_add_f32 v[186:187], v[186:187], v[200:201]
	v_pk_add_f32 v[188:189], v[188:189], v[202:203]
	v_cvt_pk_f16_f32 v52, v182, v183
	v_cvt_pk_f16_f32 v53, v184, v185
	v_cvt_pk_f16_f32 v54, v186, v187
	v_cvt_pk_f16_f32 v55, v188, v189
	global_store_dwordx4 v[236:237], v[52:55], off offset:256 sc1
	s_waitcnt vmcnt(14)
	v_add_u32_e32 v238, 144, v176
	v_lshlrev_b32_e32 v240, 11, v238
	v_lshl_add_u64 v[236:237], v[180:181], 0, v[240:241]
	v_cvt_f32_f16_e32 v182, v110
	v_cvt_f32_f16_sdwa v183, v110 dst_sel:DWORD dst_unused:UNUSED_PAD src0_sel:WORD_1
	v_cvt_f32_f16_e32 v184, v111
	v_cvt_f32_f16_sdwa v185, v111 dst_sel:DWORD dst_unused:UNUSED_PAD src0_sel:WORD_1
	v_cvt_f32_f16_e32 v186, v112
	v_cvt_f32_f16_sdwa v187, v112 dst_sel:DWORD dst_unused:UNUSED_PAD src0_sel:WORD_1
	v_cvt_f32_f16_e32 v188, v113
	v_cvt_f32_f16_sdwa v189, v113 dst_sel:DWORD dst_unused:UNUSED_PAD src0_sel:WORD_1
	v_cvt_f32_f16_e32 v196, v102
	v_cvt_f32_f16_sdwa v197, v102 dst_sel:DWORD dst_unused:UNUSED_PAD src0_sel:WORD_1
	v_cvt_f32_f16_e32 v198, v103
	v_cvt_f32_f16_sdwa v199, v103 dst_sel:DWORD dst_unused:UNUSED_PAD src0_sel:WORD_1
	v_cvt_f32_f16_e32 v200, v104
	v_cvt_f32_f16_sdwa v201, v104 dst_sel:DWORD dst_unused:UNUSED_PAD src0_sel:WORD_1
	v_cvt_f32_f16_e32 v202, v105
	v_cvt_f32_f16_sdwa v203, v105 dst_sel:DWORD dst_unused:UNUSED_PAD src0_sel:WORD_1
	v_pk_mul_f32 v[182:183], v[44:45], v[182:183]
	v_pk_mul_f32 v[184:185], v[46:47], v[184:185]
	v_pk_mul_f32 v[186:187], v[40:41], v[186:187]
	v_pk_mul_f32 v[188:189], v[42:43], v[188:189]
	v_pk_add_f32 v[182:183], v[182:183], v[196:197]
	v_pk_add_f32 v[184:185], v[184:185], v[198:199]
	v_pk_add_f32 v[186:187], v[186:187], v[200:201]
	v_pk_add_f32 v[188:189], v[188:189], v[202:203]
	v_cvt_pk_f16_f32 v44, v182, v183
	v_cvt_pk_f16_f32 v45, v184, v185
	v_cvt_pk_f16_f32 v46, v186, v187
	v_cvt_pk_f16_f32 v47, v188, v189
	global_store_dwordx4 v[236:237], v[44:47], off sc1
	v_cvt_f32_f16_e32 v182, v106
	v_cvt_f32_f16_sdwa v183, v106 dst_sel:DWORD dst_unused:UNUSED_PAD src0_sel:WORD_1
	v_cvt_f32_f16_e32 v184, v107
	v_cvt_f32_f16_sdwa v185, v107 dst_sel:DWORD dst_unused:UNUSED_PAD src0_sel:WORD_1
	v_cvt_f32_f16_e32 v186, v108
	v_cvt_f32_f16_sdwa v187, v108 dst_sel:DWORD dst_unused:UNUSED_PAD src0_sel:WORD_1
	v_cvt_f32_f16_e32 v188, v109
	v_cvt_f32_f16_sdwa v189, v109 dst_sel:DWORD dst_unused:UNUSED_PAD src0_sel:WORD_1
	v_cvt_f32_f16_e32 v196, v98
	v_cvt_f32_f16_sdwa v197, v98 dst_sel:DWORD dst_unused:UNUSED_PAD src0_sel:WORD_1
	v_cvt_f32_f16_e32 v198, v99
	v_cvt_f32_f16_sdwa v199, v99 dst_sel:DWORD dst_unused:UNUSED_PAD src0_sel:WORD_1
	v_cvt_f32_f16_e32 v200, v100
	v_cvt_f32_f16_sdwa v201, v100 dst_sel:DWORD dst_unused:UNUSED_PAD src0_sel:WORD_1
	v_cvt_f32_f16_e32 v202, v101
	v_cvt_f32_f16_sdwa v203, v101 dst_sel:DWORD dst_unused:UNUSED_PAD src0_sel:WORD_1
	v_pk_mul_f32 v[182:183], v[28:29], v[182:183]
	v_pk_mul_f32 v[184:185], v[30:31], v[184:185]
	v_pk_mul_f32 v[186:187], v[24:25], v[186:187]
	v_pk_mul_f32 v[188:189], v[26:27], v[188:189]
	v_pk_add_f32 v[182:183], v[182:183], v[196:197]
	v_pk_add_f32 v[184:185], v[184:185], v[198:199]
	v_pk_add_f32 v[186:187], v[186:187], v[200:201]
	v_pk_add_f32 v[188:189], v[188:189], v[202:203]
	v_cvt_pk_f16_f32 v28, v182, v183
	v_cvt_pk_f16_f32 v29, v184, v185
	v_cvt_pk_f16_f32 v30, v186, v187
	v_cvt_pk_f16_f32 v31, v188, v189
	global_store_dwordx4 v[236:237], v[28:31], off offset:256 sc1
	s_waitcnt vmcnt(10)
; __device__ __forceinline__ unsigned cvt_pk_f16(float lo, float hi) { f32x2 v = {lo, hi}; h16x2 b = __builtin_convertvector(v, h16x2); return __builtin_bit_cast(unsigned, b); }
;     __device__ __forceinline__ void operator()(const f32x4 (&acc)[2][2][4][2], const Unit& u, int wr, int wc, int fr, int fq) const {
;     ...
;                 for (int mp = 0; mp < 2; ++mp) {
;                     h16x8 gv[2][2], pv[2][2];
; #pragma unroll
;                     for (int mm = 0; mm < 2; ++mm)
; #pragma unroll
;                         for (int bj = 0; bj < 2; ++bj) { const size_t row = (size_t)(row0 + ai * HALF + (2 * mp + mm) * 16);
;                             gv[mm][bj] = *(const h16x8*)(Gn + row * ldg + bj * HALF);
;                             if (n > 0) pv[mm][bj] = *(const h16x8*)(Mg + row * 1024 + col0 + bj * HALF); }
; #pragma unroll
;                     for (int mm = 0; mm < 2; ++mm)
; #pragma unroll
;                         for (int bj = 0; bj < 2; ++bj) { const int m = 2 * mp + mm; const size_t row = (size_t)(row0 + ai * HALF + m * 16);
;                             float o[8];
; #pragma unroll
;                             for (int e = 0; e < 8; ++e) { const float a = e < 4 ? acc[ai][bj][m][0][e] : acc[ai][bj][m][1][e - 4]; o[e] = a * (float)gv[mm][bj][e]; }
;                             if (n > 0) {
; #pragma unroll
;                                 for (int e = 0; e < 8; ++e) o[e] += (float)pv[mm][bj][e]; }
;                             u32x4 w; w.x = cvt_pk_f16(o[0], o[1]); w.y = cvt_pk_f16(o[2], o[3]); w.z = cvt_pk_f16(o[4], o[5]); w.w = cvt_pk_f16(o[6], o[7]);
;                             *(u32x4*)(Mg + row * 1024 + col0 + bj * HALF) = w; }
	v_add_u32_e32 v238, 160, v176
	v_lshlrev_b32_e32 v240, 11, v238
	v_lshl_add_u64 v[236:237], v[180:181], 0, v[240:241]
	v_cvt_f32_f16_e32 v182, v130
	v_cvt_f32_f16_sdwa v183, v130 dst_sel:DWORD dst_unused:UNUSED_PAD src0_sel:WORD_1
	v_cvt_f32_f16_e32 v184, v131
	v_cvt_f32_f16_sdwa v185, v131 dst_sel:DWORD dst_unused:UNUSED_PAD src0_sel:WORD_1
	v_cvt_f32_f16_e32 v186, v132
	v_cvt_f32_f16_sdwa v187, v132 dst_sel:DWORD dst_unused:UNUSED_PAD src0_sel:WORD_1
	v_cvt_f32_f16_e32 v188, v133
	v_cvt_f32_f16_sdwa v189, v133 dst_sel:DWORD dst_unused:UNUSED_PAD src0_sel:WORD_1
	v_cvt_f32_f16_e32 v196, v138
	v_cvt_f32_f16_sdwa v197, v138 dst_sel:DWORD dst_unused:UNUSED_PAD src0_sel:WORD_1
	v_cvt_f32_f16_e32 v198, v139
	v_cvt_f32_f16_sdwa v199, v139 dst_sel:DWORD dst_unused:UNUSED_PAD src0_sel:WORD_1
	v_cvt_f32_f16_e32 v200, v140
	v_cvt_f32_f16_sdwa v201, v140 dst_sel:DWORD dst_unused:UNUSED_PAD src0_sel:WORD_1
	v_cvt_f32_f16_e32 v202, v141
	v_cvt_f32_f16_sdwa v203, v141 dst_sel:DWORD dst_unused:UNUSED_PAD src0_sel:WORD_1
	v_pk_mul_f32 v[182:183], v[20:21], v[182:183]
	v_pk_mul_f32 v[184:185], v[22:23], v[184:185]
	v_pk_mul_f32 v[186:187], v[16:17], v[186:187]
	v_pk_mul_f32 v[188:189], v[18:19], v[188:189]
	v_pk_add_f32 v[182:183], v[182:183], v[196:197]
	v_pk_add_f32 v[184:185], v[184:185], v[198:199]
	v_pk_add_f32 v[186:187], v[186:187], v[200:201]
	v_pk_add_f32 v[188:189], v[188:189], v[202:203]
	v_cvt_pk_f16_f32 v20, v182, v183
	v_cvt_pk_f16_f32 v21, v184, v185
	v_cvt_pk_f16_f32 v22, v186, v187
	v_cvt_pk_f16_f32 v23, v188, v189
	global_store_dwordx4 v[236:237], v[20:23], off sc1
	v_cvt_f32_f16_e32 v182, v134
	v_cvt_f32_f16_sdwa v183, v134 dst_sel:DWORD dst_unused:UNUSED_PAD src0_sel:WORD_1
	v_cvt_f32_f16_e32 v184, v135
	v_cvt_f32_f16_sdwa v185, v135 dst_sel:DWORD dst_unused:UNUSED_PAD src0_sel:WORD_1
	v_cvt_f32_f16_e32 v186, v136
	v_cvt_f32_f16_sdwa v187, v136 dst_sel:DWORD dst_unused:UNUSED_PAD src0_sel:WORD_1
	v_cvt_f32_f16_e32 v188, v137
	v_cvt_f32_f16_sdwa v189, v137 dst_sel:DWORD dst_unused:UNUSED_PAD src0_sel:WORD_1
	v_cvt_f32_f16_e32 v196, v142
	v_cvt_f32_f16_sdwa v197, v142 dst_sel:DWORD dst_unused:UNUSED_PAD src0_sel:WORD_1
	v_cvt_f32_f16_e32 v198, v143
	v_cvt_f32_f16_sdwa v199, v143 dst_sel:DWORD dst_unused:UNUSED_PAD src0_sel:WORD_1
	v_cvt_f32_f16_e32 v200, v144
	v_cvt_f32_f16_sdwa v201, v144 dst_sel:DWORD dst_unused:UNUSED_PAD src0_sel:WORD_1
	v_cvt_f32_f16_e32 v202, v145
	v_cvt_f32_f16_sdwa v203, v145 dst_sel:DWORD dst_unused:UNUSED_PAD src0_sel:WORD_1
	v_pk_mul_f32 v[182:183], v[32:33], v[182:183]
	v_pk_mul_f32 v[184:185], v[34:35], v[184:185]
	v_pk_mul_f32 v[186:187], v[36:37], v[186:187]
	v_pk_mul_f32 v[188:189], v[38:39], v[188:189]
	v_pk_add_f32 v[182:183], v[182:183], v[196:197]
	v_pk_add_f32 v[184:185], v[184:185], v[198:199]
	v_pk_add_f32 v[186:187], v[186:187], v[200:201]
	v_pk_add_f32 v[188:189], v[188:189], v[202:203]
	v_cvt_pk_f16_f32 v32, v182, v183
	v_cvt_pk_f16_f32 v33, v184, v185
	v_cvt_pk_f16_f32 v34, v186, v187
	v_cvt_pk_f16_f32 v35, v188, v189
	global_store_dwordx4 v[236:237], v[32:35], off offset:256 sc1
	s_waitcnt vmcnt(8)
	v_add_u32_e32 v238, 176, v176
	v_lshlrev_b32_e32 v240, 11, v238
	v_lshl_add_u64 v[236:237], v[180:181], 0, v[240:241]
	v_cvt_f32_f16_e32 v182, v92
	v_cvt_f32_f16_sdwa v183, v92 dst_sel:DWORD dst_unused:UNUSED_PAD src0_sel:WORD_1
	v_cvt_f32_f16_e32 v184, v93
	v_cvt_f32_f16_sdwa v185, v93 dst_sel:DWORD dst_unused:UNUSED_PAD src0_sel:WORD_1
	v_cvt_f32_f16_e32 v186, v94
	v_cvt_f32_f16_sdwa v187, v94 dst_sel:DWORD dst_unused:UNUSED_PAD src0_sel:WORD_1
	v_cvt_f32_f16_e32 v188, v95
	v_cvt_f32_f16_sdwa v189, v95 dst_sel:DWORD dst_unused:UNUSED_PAD src0_sel:WORD_1
	v_cvt_f32_f16_e32 v196, v84
	v_cvt_f32_f16_sdwa v197, v84 dst_sel:DWORD dst_unused:UNUSED_PAD src0_sel:WORD_1
	v_cvt_f32_f16_e32 v198, v85
	v_cvt_f32_f16_sdwa v199, v85 dst_sel:DWORD dst_unused:UNUSED_PAD src0_sel:WORD_1
	v_cvt_f32_f16_e32 v200, v86
	v_cvt_f32_f16_sdwa v201, v86 dst_sel:DWORD dst_unused:UNUSED_PAD src0_sel:WORD_1
	v_cvt_f32_f16_e32 v202, v87
	v_cvt_f32_f16_sdwa v203, v87 dst_sel:DWORD dst_unused:UNUSED_PAD src0_sel:WORD_1
	v_pk_mul_f32 v[182:183], v[4:5], v[182:183]
	v_pk_mul_f32 v[184:185], v[6:7], v[184:185]
	v_pk_mul_f32 v[186:187], v[0:1], v[186:187]
	v_pk_mul_f32 v[188:189], v[2:3], v[188:189]
	v_pk_add_f32 v[182:183], v[182:183], v[196:197]
	v_pk_add_f32 v[184:185], v[184:185], v[198:199]
	v_pk_add_f32 v[186:187], v[186:187], v[200:201]
	v_pk_add_f32 v[188:189], v[188:189], v[202:203]
	v_cvt_pk_f16_f32 v4, v182, v183
	v_cvt_pk_f16_f32 v5, v184, v185
	v_cvt_pk_f16_f32 v6, v186, v187
	v_cvt_pk_f16_f32 v7, v188, v189
	global_store_dwordx4 v[236:237], v[4:7], off sc1
	v_cvt_f32_f16_e32 v182, v88
	v_cvt_f32_f16_sdwa v183, v88 dst_sel:DWORD dst_unused:UNUSED_PAD src0_sel:WORD_1
	v_cvt_f32_f16_e32 v184, v89
	v_cvt_f32_f16_sdwa v185, v89 dst_sel:DWORD dst_unused:UNUSED_PAD src0_sel:WORD_1
	v_cvt_f32_f16_e32 v186, v90
	v_cvt_f32_f16_sdwa v187, v90 dst_sel:DWORD dst_unused:UNUSED_PAD src0_sel:WORD_1
	v_cvt_f32_f16_e32 v188, v91
	v_cvt_f32_f16_sdwa v189, v91 dst_sel:DWORD dst_unused:UNUSED_PAD src0_sel:WORD_1
	v_cvt_f32_f16_e32 v196, v80
	v_cvt_f32_f16_sdwa v197, v80 dst_sel:DWORD dst_unused:UNUSED_PAD src0_sel:WORD_1
	v_cvt_f32_f16_e32 v198, v81
	v_cvt_f32_f16_sdwa v199, v81 dst_sel:DWORD dst_unused:UNUSED_PAD src0_sel:WORD_1
	v_cvt_f32_f16_e32 v200, v82
	v_cvt_f32_f16_sdwa v201, v82 dst_sel:DWORD dst_unused:UNUSED_PAD src0_sel:WORD_1
	v_cvt_f32_f16_e32 v202, v83
	v_cvt_f32_f16_sdwa v203, v83 dst_sel:DWORD dst_unused:UNUSED_PAD src0_sel:WORD_1
	v_pk_mul_f32 v[182:183], v[8:9], v[182:183]
	v_pk_mul_f32 v[184:185], v[10:11], v[184:185]
	v_pk_mul_f32 v[186:187], v[12:13], v[186:187]
	v_pk_mul_f32 v[188:189], v[14:15], v[188:189]
	v_pk_add_f32 v[182:183], v[182:183], v[196:197]
	v_pk_add_f32 v[184:185], v[184:185], v[198:199]
	v_pk_add_f32 v[186:187], v[186:187], v[200:201]
	v_pk_add_f32 v[188:189], v[188:189], v[202:203]
	v_cvt_pk_f16_f32 v8, v182, v183
	v_cvt_pk_f16_f32 v9, v184, v185
	v_cvt_pk_f16_f32 v10, v186, v187
	v_cvt_pk_f16_f32 v11, v188, v189
	global_store_dwordx4 v[236:237], v[8:11], off offset:256 sc1
	s_branch .Lbrepi_done
